# PEER coefficient phase written by hand: 3-stage software pipeline over a thread's 8 passes (streaming loads two ahead, scale gathers one ahead), four entries interleaved, both erf ranges evaluated and
# speedup vs baseline: 1.0001x; 1.0001x over previous
; DI int tidx() { int t = threadIdx.x & 255; asm volatile("" : "+v"(t)); return t; }
; DI float bflo(unsigned u) { return __uint_as_float(u << 16); }
; DI float bfhi(unsigned u) { return __uint_as_float(u & 0xffff0000u); }
; DI void phase_peercoef(const Params& p, int bid, int nb) {
;   const bf16_t* pd = (const bf16_t*)(p.ws + WS_PD);
;   const int* eidx = (const int*)(p.ws + WS_EIDX); const float* gate = (const float*)(p.ws + WS_GATE);
;   const float* uinv = (const float*)(p.ws + WS_UINV); const float* vinv = (const float*)(p.ws + WS_VINV);
;   float* coef = (float*)(p.ws + WS_COEF);
;   for (size_t i4 = ((size_t)bid * NT + tidx()) * 4; i4 < (size_t)T_ * 128; i4 += (size_t)nb * NT * 4) {
;     f32x4 d = {0.f, 0.f, 0.f, 0.f};
; #pragma unroll
;     for (int x = 0; x < 8; ++x) { const u32x2 pb = *(const u32x2*)(pd + (size_t)x * T_ * 128 + i4); d += (f32x4){bflo(pb[0]), bfhi(pb[0]), bflo(pb[1]), bfhi(pb[1])}; }
;     typedef int i32x4 __attribute__((ext_vector_type(4)));
;     const i32x4 e = *(const i32x4*)(eidx + i4); const f32x4 g = *(const f32x4*)(gate + i4);
.LBB0_1805:
	s_or_b64 exec, exec, s[0:1]
	s_waitcnt lgkmcnt(0)
	v_mov_b32_e32 v0, v206
	s_barrier
	v_lshlrev_b64 v[2:3], 10, v[176:177]
	v_ashrrev_i32_e32 v1, 31, v0
	v_lshl_add_u64 v[8:9], v[0:1], 2, v[2:3]
	s_mov_b64 s[0:1], 0x400000
	v_cmp_gt_u64_e32 vcc, s[0:1], v[8:9]
	s_and_saveexec_b64 s[20:21], vcc
	s_cbranch_execz .LBB0_1824
	v_lshlrev_b32_e32 v12, 10, v176
	v_lshl_add_u32 v12, v206, 2, v12
	v_lshlrev_b32_e32 v10, 1, v12
	v_lshlrev_b32_e32 v11, 2, v12
	s_add_u32 s0, s84, 0x14000000
	s_addc_u32 s1, s85, 0
	s_add_u32 s2, s84, 0x14800000
	s_addc_u32 s3, s85, 0
	s_add_u32 s4, s84, 0x15000000
	s_addc_u32 s5, s85, 0
	s_add_u32 s6, s84, 0x15800000
	s_addc_u32 s7, s85, 0
	s_add_u32 s8, s84, 0x16000000
	s_addc_u32 s9, s85, 0
	s_add_u32 s10, s84, 0x16800000
	s_addc_u32 s11, s85, 0
	s_add_u32 s12, s84, 0x17000000
	s_addc_u32 s13, s85, 0
	s_add_u32 s14, s84, 0x17800000
	s_addc_u32 s15, s85, 0
	s_add_u32 s22, s84, 0x12000000
	s_addc_u32 s23, s85, 0
	s_add_u32 s24, s84, 0x13000000
	s_addc_u32 s25, s85, 0
	s_add_u32 s26, s84, 0x2000000
	s_addc_u32 s27, s85, 0
	s_add_u32 s28, s84, 0x10000000
	s_addc_u32 s29, s85, 0
	s_mov_b32 s38, 0x378e98ab
	s_mov_b32 s39, 0x3b7cd369
	s_mov_b32 s40, 0xbcc618b2
	s_mov_b32 s41, 0x3dda74e4
	s_mov_b32 s42, 0x3f228afd
	s_mov_b32 s43, 0x3e03c728
	s_mov_b32 s44, 0xbfb8aa3b
	s_mov_b32 s45, 0x42ce8ed0
	s_mov_b32 s46, 0xc2b17218
	s_brev_b32 s47, -2
	v_mov_b32_e32 v4, 0x3ba10414
	v_mov_b32_e32 v5, 0xb9c68948
	v_mov_b32_e32 v6, 0x7f800000
	v_mov_b32_e32 v104, v10
	v_mov_b32_e32 v107, v11
	global_load_dwordx4 v[32:35], v107, s[22:23]
	global_load_dwordx2 v[16:17], v104, s[0:1]
	global_load_dwordx2 v[18:19], v104, s[2:3]
	global_load_dwordx2 v[20:21], v104, s[4:5]
	global_load_dwordx2 v[22:23], v104, s[6:7]
	global_load_dwordx2 v[24:25], v104, s[8:9]
	global_load_dwordx2 v[26:27], v104, s[10:11]
	global_load_dwordx2 v[28:29], v104, s[12:13]
	global_load_dwordx2 v[30:31], v104, s[14:15]
	global_load_dwordx4 v[36:39], v107, s[24:25]
	v_add_u32_e32 v105, 0x100000, v10
	v_add_u32_e32 v108, 0x200000, v11
	global_load_dwordx4 v[56:59], v108, s[22:23]
	global_load_dwordx2 v[40:41], v105, s[0:1]
	global_load_dwordx2 v[42:43], v105, s[2:3]
	global_load_dwordx2 v[44:45], v105, s[4:5]
	global_load_dwordx2 v[46:47], v105, s[6:7]
	global_load_dwordx2 v[48:49], v105, s[8:9]
	global_load_dwordx2 v[50:51], v105, s[10:11]
	global_load_dwordx2 v[52:53], v105, s[12:13]
	global_load_dwordx2 v[54:55], v105, s[14:15]
	global_load_dwordx4 v[60:63], v108, s[24:25]
	s_waitcnt vmcnt(10)
	v_lshlrev_b32_e32 v112, 2, v32
	v_lshlrev_b32_e32 v113, 2, v33
	v_lshlrev_b32_e32 v114, 2, v34
	v_lshlrev_b32_e32 v115, 2, v35
	global_load_dword v88, v112, s[28:29]
	global_load_dword v89, v113, s[28:29]
	global_load_dword v90, v114, s[28:29]
	global_load_dword v91, v115, s[28:29]
	v_add_u32_e32 v116, 0x10000, v112
	v_add_u32_e32 v117, 0x10000, v113
	v_add_u32_e32 v118, 0x10000, v114
	v_add_u32_e32 v119, 0x10000, v115
	global_load_dword v92, v116, s[28:29]
	global_load_dword v93, v117, s[28:29]
	global_load_dword v94, v118, s[28:29]
	global_load_dword v95, v119, s[28:29]
	v_add_u32_e32 v106, 0x200000, v10
	v_add_u32_e32 v109, 0x400000, v11
	global_load_dwordx4 v[80:83], v109, s[22:23]
	global_load_dwordx2 v[64:65], v106, s[0:1]
	global_load_dwordx2 v[66:67], v106, s[2:3]
	global_load_dwordx2 v[68:69], v106, s[4:5]
	global_load_dwordx2 v[70:71], v106, s[6:7]
	global_load_dwordx2 v[72:73], v106, s[8:9]
	global_load_dwordx2 v[74:75], v106, s[10:11]
	global_load_dwordx2 v[76:77], v106, s[12:13]
	global_load_dwordx2 v[78:79], v106, s[14:15]
	global_load_dwordx4 v[84:87], v109, s[24:25]
	s_waitcnt vmcnt(18)
	v_lshlrev_b32_e32 v112, 2, v56
	v_lshlrev_b32_e32 v113, 2, v57
	v_lshlrev_b32_e32 v114, 2, v58
	v_lshlrev_b32_e32 v115, 2, v59
	global_load_dword v96, v112, s[28:29]
	global_load_dword v97, v113, s[28:29]
	global_load_dword v98, v114, s[28:29]
	global_load_dword v99, v115, s[28:29]
	v_add_u32_e32 v116, 0x10000, v112
	v_add_u32_e32 v117, 0x10000, v113
	v_add_u32_e32 v118, 0x10000, v114
	v_add_u32_e32 v119, 0x10000, v115
	global_load_dword v100, v116, s[28:29]
	global_load_dword v101, v117, s[28:29]
	global_load_dword v102, v118, s[28:29]
	global_load_dword v103, v119, s[28:29]
	s_waitcnt vmcnt(18)
; DI float bflo(unsigned u) { return __uint_as_float(u << 16); }
; DI float bfhi(unsigned u) { return __uint_as_float(u & 0xffff0000u); }
; DI void phase_peercoef(const Params& p, int bid, int nb) {
;     ...
;     for (int x = 0; x < 8; ++x) { const u32x2 pb = *(const u32x2*)(pd + (size_t)x * T_ * 128 + i4); d += (f32x4){bflo(pb[0]), bfhi(pb[0]), bflo(pb[1]), bfhi(pb[1])}; }
;     typedef int i32x4 __attribute__((ext_vector_type(4)));
;     const i32x4 e = *(const i32x4*)(eidx + i4); const f32x4 g = *(const f32x4*)(gate + i4);
;     f32x4 o;
; #pragma unroll
;     for (int k = 0; k < 4; ++k) { const float dk = d[k] * uinv[e[k]]; o[k] = g[k] * 0.5f * dk * (1.f + erff(dk * 0.70710678118654752f)) * vinv[e[k]]; }
	v_lshlrev_b32_e32 v124, 16, v16
	v_and_b32_e32 v125, 0xffff0000, v16
	v_pk_add_f32 v[120:121], v[124:125], 0 op_sel_hi:[1,0]
	v_lshlrev_b32_e32 v124, 16, v18
	v_and_b32_e32 v125, 0xffff0000, v18
	v_pk_add_f32 v[120:121], v[120:121], v[124:125]
	v_lshlrev_b32_e32 v124, 16, v20
	v_and_b32_e32 v125, 0xffff0000, v20
	v_pk_add_f32 v[120:121], v[120:121], v[124:125]
	v_lshlrev_b32_e32 v124, 16, v22
	v_and_b32_e32 v125, 0xffff0000, v22
	v_pk_add_f32 v[120:121], v[120:121], v[124:125]
	v_lshlrev_b32_e32 v124, 16, v24
	v_and_b32_e32 v125, 0xffff0000, v24
	v_pk_add_f32 v[120:121], v[120:121], v[124:125]
	v_lshlrev_b32_e32 v124, 16, v26
	v_and_b32_e32 v125, 0xffff0000, v26
	v_pk_add_f32 v[120:121], v[120:121], v[124:125]
	v_lshlrev_b32_e32 v124, 16, v28
	v_and_b32_e32 v125, 0xffff0000, v28
	v_pk_add_f32 v[120:121], v[120:121], v[124:125]
	v_lshlrev_b32_e32 v124, 16, v30
	v_and_b32_e32 v125, 0xffff0000, v30
	v_pk_add_f32 v[120:121], v[120:121], v[124:125]
	v_lshlrev_b32_e32 v124, 16, v17
	v_and_b32_e32 v125, 0xffff0000, v17
	v_pk_add_f32 v[122:123], v[124:125], 0 op_sel_hi:[1,0]
	v_lshlrev_b32_e32 v124, 16, v19
	v_and_b32_e32 v125, 0xffff0000, v19
	v_pk_add_f32 v[122:123], v[122:123], v[124:125]
	v_lshlrev_b32_e32 v124, 16, v21
	v_and_b32_e32 v125, 0xffff0000, v21
	v_pk_add_f32 v[122:123], v[122:123], v[124:125]
	v_lshlrev_b32_e32 v124, 16, v23
	v_and_b32_e32 v125, 0xffff0000, v23
	v_pk_add_f32 v[122:123], v[122:123], v[124:125]
	v_lshlrev_b32_e32 v124, 16, v25
	v_and_b32_e32 v125, 0xffff0000, v25
	v_pk_add_f32 v[122:123], v[122:123], v[124:125]
	v_lshlrev_b32_e32 v124, 16, v27
	v_and_b32_e32 v125, 0xffff0000, v27
	v_pk_add_f32 v[122:123], v[122:123], v[124:125]
	v_lshlrev_b32_e32 v124, 16, v29
	v_and_b32_e32 v125, 0xffff0000, v29
	v_pk_add_f32 v[122:123], v[122:123], v[124:125]
	v_lshlrev_b32_e32 v124, 16, v31
	v_and_b32_e32 v125, 0xffff0000, v31
	v_pk_add_f32 v[122:123], v[122:123], v[124:125]
	v_mul_f32_e32 v128, v88, v120
	v_mul_f32_e32 v129, v89, v121
	v_mul_f32_e32 v130, v90, v122
	v_mul_f32_e32 v131, v91, v123
	v_mul_f32_e32 v132, 0x3f3504f3, v128
	v_mul_f32_e32 v133, 0x3f3504f3, v129
	v_mul_f32_e32 v134, 0x3f3504f3, v130
	v_mul_f32_e32 v135, 0x3f3504f3, v131
	v_fma_f32 v136, |v132|, s38, v5
	v_fma_f32 v137, |v133|, s38, v5
	v_fma_f32 v138, |v134|, s38, v5
	v_fma_f32 v139, |v135|, s38, v5
	v_fma_f32 v136, |v132|, v136, s39
	v_fma_f32 v137, |v133|, v137, s39
	v_fma_f32 v138, |v134|, v138, s39
	v_fma_f32 v139, |v135|, v139, s39
	v_fma_f32 v136, |v132|, v136, s40
	v_fma_f32 v137, |v133|, v137, s40
	v_fma_f32 v138, |v134|, v138, s40
	v_fma_f32 v139, |v135|, v139, s40
	v_fma_f32 v136, |v132|, v136, s41
	v_fma_f32 v137, |v133|, v137, s41
	v_fma_f32 v138, |v134|, v138, s41
	v_fma_f32 v139, |v135|, v139, s41
	v_fma_f32 v136, |v132|, v136, s42
	v_fma_f32 v137, |v133|, v137, s42
	v_fma_f32 v138, |v134|, v138, s42
	v_fma_f32 v139, |v135|, v139, s42
	v_fma_f32 v136, |v132|, v136, s43
	v_fma_f32 v137, |v133|, v137, s43
	v_fma_f32 v138, |v134|, v138, s43
	v_fma_f32 v139, |v135|, v139, s43
	v_fma_f32 v136, |v132|, v136, |v132|
	v_fma_f32 v137, |v133|, v137, |v133|
	v_fma_f32 v138, |v134|, v138, |v134|
	v_fma_f32 v139, |v135|, v139, |v135|
	v_mul_f32_e32 v140, 0xbfb8aa3b, v136
	v_mul_f32_e32 v141, 0xbfb8aa3b, v137
	v_mul_f32_e32 v142, 0xbfb8aa3b, v138
	v_mul_f32_e32 v143, 0xbfb8aa3b, v139
	v_fma_f32 v144, v136, s44, -v140
	v_fma_f32 v145, v137, s44, -v141
	v_fma_f32 v148, v138, s44, -v142
	v_fma_f32 v149, v139, s44, -v143
	v_rndne_f32_e32 v150, v140
	v_rndne_f32_e32 v151, v141
	v_rndne_f32_e32 v152, v142
	v_rndne_f32_e32 v153, v143
	v_fmac_f32_e32 v144, 0xb2a5705f, v136
	v_fmac_f32_e32 v145, 0xb2a5705f, v137
	v_fmac_f32_e32 v148, 0xb2a5705f, v138
	v_fmac_f32_e32 v149, 0xb2a5705f, v139
	v_sub_f32_e32 v140, v140, v150
	v_sub_f32_e32 v141, v141, v151
	v_sub_f32_e32 v142, v142, v152
	v_sub_f32_e32 v143, v143, v153
	v_add_f32_e32 v140, v140, v144
	v_add_f32_e32 v141, v141, v145
	v_add_f32_e32 v142, v142, v148
	v_add_f32_e32 v143, v143, v149
	v_cvt_i32_f32_e32 v150, v150
	v_cvt_i32_f32_e32 v151, v151
	v_cvt_i32_f32_e32 v152, v152
	v_cvt_i32_f32_e32 v153, v153
	v_exp_f32_e32 v140, v140
	v_exp_f32_e32 v141, v141
	v_exp_f32_e32 v142, v142
	v_exp_f32_e32 v143, v143
	v_cmp_nlt_f32_e64 vcc, s45, v136
	v_cmp_nlt_f32_e64 s[30:31], s45, v137
	v_cmp_nlt_f32_e64 s[34:35], s45, v138
	v_cmp_nlt_f32_e64 s[36:37], s45, v139
	v_ldexp_f32 v140, v140, v150
	v_ldexp_f32 v141, v141, v151
	v_ldexp_f32 v142, v142, v152
	v_ldexp_f32 v143, v143, v153
	v_cndmask_b32_e64 v140, 0, v140, vcc
	v_cndmask_b32_e64 v141, 0, v141, s[30:31]
	v_cndmask_b32_e64 v142, 0, v142, s[34:35]
	v_cndmask_b32_e64 v143, 0, v143, s[36:37]
	v_cmp_ngt_f32_e64 vcc, s46, v136
	v_cmp_ngt_f32_e64 s[30:31], s46, v137
	v_cmp_ngt_f32_e64 s[34:35], s46, v138
	v_cmp_ngt_f32_e64 s[36:37], s46, v139
	v_mul_f32_e32 v158, v132, v132
	v_mul_f32_e32 v159, v133, v133
	v_mul_f32_e32 v160, v134, v134
	v_mul_f32_e32 v161, v135, v135
	v_fmamk_f32 v154, v158, 0xba1345e1, v4
	v_fmamk_f32 v155, v159, 0xba1345e1, v4
	v_fmamk_f32 v156, v160, 0xba1345e1, v4
	v_fmamk_f32 v157, v161, 0xba1345e1, v4
	v_cndmask_b32_e64 v140, v6, v140, vcc
	v_cndmask_b32_e64 v141, v6, v141, s[30:31]
	v_cndmask_b32_e64 v142, v6, v142, s[34:35]
	v_cndmask_b32_e64 v143, v6, v143, s[36:37]
	v_sub_f32_e32 v162, 1.0, v140
	v_sub_f32_e32 v163, 1.0, v141
	v_sub_f32_e32 v164, 1.0, v142
	v_sub_f32_e32 v165, 1.0, v143
	v_fmaak_f32 v154, v158, v154, 0xbcdac9b8
	v_fmaak_f32 v155, v159, v155, 0xbcdac9b8
	v_fmaak_f32 v156, v160, v156, 0xbcdac9b8
	v_fmaak_f32 v157, v161, v157, 0xbcdac9b8
	v_fmaak_f32 v154, v158, v154, 0x3de703be
	v_fmaak_f32 v155, v159, v155, 0x3de703be
; DI float bflo(unsigned u) { return __uint_as_float(u << 16); }
; DI float bfhi(unsigned u) { return __uint_as_float(u & 0xffff0000u); }
; DI void phase_peercoef(const Params& p, int bid, int nb) {
;     ...
;     for (int x = 0; x < 8; ++x) { const u32x2 pb = *(const u32x2*)(pd + (size_t)x * T_ * 128 + i4); d += (f32x4){bflo(pb[0]), bfhi(pb[0]), bflo(pb[1]), bfhi(pb[1])}; }
;     typedef int i32x4 __attribute__((ext_vector_type(4)));
;     const i32x4 e = *(const i32x4*)(eidx + i4); const f32x4 g = *(const f32x4*)(gate + i4);
;     ...
; #pragma unroll
;     for (int k = 0; k < 4; ++k) { const float dk = d[k] * uinv[e[k]]; o[k] = g[k] * 0.5f * dk * (1.f + erff(dk * 0.70710678118654752f)) * vinv[e[k]]; }
;     *(f32x4*)(coef + i4) = o;
	v_fmaak_f32 v156, v160, v156, 0x3de703be
	v_fmaak_f32 v157, v161, v157, 0x3de703be
	v_fmaak_f32 v154, v158, v154, 0xbec09330
	v_fmaak_f32 v155, v159, v155, 0xbec09330
	v_fmaak_f32 v156, v160, v156, 0xbec09330
	v_fmaak_f32 v157, v161, v157, 0xbec09330
	v_fmaak_f32 v158, v158, v154, 0x3e0375d0
	v_fmaak_f32 v159, v159, v155, 0x3e0375d0
	v_fmaak_f32 v160, v160, v156, 0x3e0375d0
	v_fmaak_f32 v161, v161, v157, 0x3e0375d0
	v_fma_f32 v154, |v132|, v158, |v132|
	v_fma_f32 v155, |v133|, v159, |v133|
	v_fma_f32 v156, |v134|, v160, |v134|
	v_fma_f32 v157, |v135|, v161, |v135|
	v_cmp_nlt_f32_e64 vcc, |v132|, 1.0
	v_cmp_nlt_f32_e64 s[30:31], |v133|, 1.0
	v_cmp_nlt_f32_e64 s[34:35], |v134|, 1.0
	v_cmp_nlt_f32_e64 s[36:37], |v135|, 1.0
	v_mul_f32_e32 v166, 0.5, v36
	v_mul_f32_e32 v167, 0.5, v37
	v_mul_f32_e32 v168, 0.5, v38
	v_mul_f32_e32 v169, 0.5, v39
	v_mul_f32_e32 v166, v166, v128
	v_mul_f32_e32 v167, v167, v129
	v_mul_f32_e32 v168, v168, v130
	v_mul_f32_e32 v169, v169, v131
	v_cndmask_b32_e64 v162, v154, v162, vcc
	v_cndmask_b32_e64 v163, v155, v163, s[30:31]
	v_cndmask_b32_e64 v164, v156, v164, s[34:35]
	v_cndmask_b32_e64 v165, v157, v165, s[36:37]
	v_bfi_b32 v162, s47, v162, v132
	v_bfi_b32 v163, s47, v163, v133
	v_bfi_b32 v164, s47, v164, v134
	v_bfi_b32 v165, s47, v165, v135
	v_add_f32_e32 v162, 1.0, v162
	v_add_f32_e32 v163, 1.0, v163
	v_add_f32_e32 v164, 1.0, v164
	v_add_f32_e32 v165, 1.0, v165
	v_mul_f32_e32 v166, v166, v162
	v_mul_f32_e32 v167, v167, v163
	v_mul_f32_e32 v168, v168, v164
	v_mul_f32_e32 v169, v169, v165
	v_mul_f32_e32 v166, v92, v166
	v_mul_f32_e32 v167, v93, v167
	v_mul_f32_e32 v168, v94, v168
	v_mul_f32_e32 v169, v95, v169
	global_store_dwordx4 v107, v[166:169], s[26:27]
	v_add_u32_e32 v104, 0x300000, v10
	v_add_u32_e32 v107, 0x600000, v11
	global_load_dwordx4 v[32:35], v107, s[22:23]
	global_load_dwordx2 v[16:17], v104, s[0:1]
	global_load_dwordx2 v[18:19], v104, s[2:3]
	global_load_dwordx2 v[20:21], v104, s[4:5]
	global_load_dwordx2 v[22:23], v104, s[6:7]
	global_load_dwordx2 v[24:25], v104, s[8:9]
	global_load_dwordx2 v[26:27], v104, s[10:11]
	global_load_dwordx2 v[28:29], v104, s[12:13]
	global_load_dwordx2 v[30:31], v104, s[14:15]
	global_load_dwordx4 v[36:39], v107, s[24:25]
	s_waitcnt vmcnt(19)
	v_lshlrev_b32_e32 v112, 2, v80
	v_lshlrev_b32_e32 v113, 2, v81
	v_lshlrev_b32_e32 v114, 2, v82
	v_lshlrev_b32_e32 v115, 2, v83
	global_load_dword v88, v112, s[28:29]
	global_load_dword v89, v113, s[28:29]
	global_load_dword v90, v114, s[28:29]
	global_load_dword v91, v115, s[28:29]
	v_add_u32_e32 v116, 0x10000, v112
	v_add_u32_e32 v117, 0x10000, v113
	v_add_u32_e32 v118, 0x10000, v114
	v_add_u32_e32 v119, 0x10000, v115
	global_load_dword v92, v116, s[28:29]
	global_load_dword v93, v117, s[28:29]
	global_load_dword v94, v118, s[28:29]
	global_load_dword v95, v119, s[28:29]
	s_waitcnt vmcnt(19)
	v_lshlrev_b32_e32 v124, 16, v40
	v_and_b32_e32 v125, 0xffff0000, v40
	v_pk_add_f32 v[120:121], v[124:125], 0 op_sel_hi:[1,0]
	v_lshlrev_b32_e32 v124, 16, v42
	v_and_b32_e32 v125, 0xffff0000, v42
	v_pk_add_f32 v[120:121], v[120:121], v[124:125]
	v_lshlrev_b32_e32 v124, 16, v44
	v_and_b32_e32 v125, 0xffff0000, v44
	v_pk_add_f32 v[120:121], v[120:121], v[124:125]
	v_lshlrev_b32_e32 v124, 16, v46
	v_and_b32_e32 v125, 0xffff0000, v46
	v_pk_add_f32 v[120:121], v[120:121], v[124:125]
	v_lshlrev_b32_e32 v124, 16, v48
	v_and_b32_e32 v125, 0xffff0000, v48
	v_pk_add_f32 v[120:121], v[120:121], v[124:125]
	v_lshlrev_b32_e32 v124, 16, v50
	v_and_b32_e32 v125, 0xffff0000, v50
	v_pk_add_f32 v[120:121], v[120:121], v[124:125]
	v_lshlrev_b32_e32 v124, 16, v52
	v_and_b32_e32 v125, 0xffff0000, v52
	v_pk_add_f32 v[120:121], v[120:121], v[124:125]
	v_lshlrev_b32_e32 v124, 16, v54
	v_and_b32_e32 v125, 0xffff0000, v54
	v_pk_add_f32 v[120:121], v[120:121], v[124:125]
	v_lshlrev_b32_e32 v124, 16, v41
	v_and_b32_e32 v125, 0xffff0000, v41
	v_pk_add_f32 v[122:123], v[124:125], 0 op_sel_hi:[1,0]
	v_lshlrev_b32_e32 v124, 16, v43
	v_and_b32_e32 v125, 0xffff0000, v43
	v_pk_add_f32 v[122:123], v[122:123], v[124:125]
	v_lshlrev_b32_e32 v124, 16, v45
	v_and_b32_e32 v125, 0xffff0000, v45
	v_pk_add_f32 v[122:123], v[122:123], v[124:125]
	v_lshlrev_b32_e32 v124, 16, v47
	v_and_b32_e32 v125, 0xffff0000, v47
	v_pk_add_f32 v[122:123], v[122:123], v[124:125]
	v_lshlrev_b32_e32 v124, 16, v49
	v_and_b32_e32 v125, 0xffff0000, v49
	v_pk_add_f32 v[122:123], v[122:123], v[124:125]
	v_lshlrev_b32_e32 v124, 16, v51
	v_and_b32_e32 v125, 0xffff0000, v51
	v_pk_add_f32 v[122:123], v[122:123], v[124:125]
	v_lshlrev_b32_e32 v124, 16, v53
	v_and_b32_e32 v125, 0xffff0000, v53
	v_pk_add_f32 v[122:123], v[122:123], v[124:125]
	v_lshlrev_b32_e32 v124, 16, v55
	v_and_b32_e32 v125, 0xffff0000, v55
	v_pk_add_f32 v[122:123], v[122:123], v[124:125]
	v_mul_f32_e32 v128, v96, v120
	v_mul_f32_e32 v129, v97, v121
	v_mul_f32_e32 v130, v98, v122
	v_mul_f32_e32 v131, v99, v123
	v_mul_f32_e32 v132, 0x3f3504f3, v128
	v_mul_f32_e32 v133, 0x3f3504f3, v129
	v_mul_f32_e32 v134, 0x3f3504f3, v130
	v_mul_f32_e32 v135, 0x3f3504f3, v131
	v_fma_f32 v136, |v132|, s38, v5
	v_fma_f32 v137, |v133|, s38, v5
	v_fma_f32 v138, |v134|, s38, v5
	v_fma_f32 v139, |v135|, s38, v5
	v_fma_f32 v136, |v132|, v136, s39
	v_fma_f32 v137, |v133|, v137, s39
	v_fma_f32 v138, |v134|, v138, s39
	v_fma_f32 v139, |v135|, v139, s39
	v_fma_f32 v136, |v132|, v136, s40
	v_fma_f32 v137, |v133|, v137, s40
	v_fma_f32 v138, |v134|, v138, s40
	v_fma_f32 v139, |v135|, v139, s40
	v_fma_f32 v136, |v132|, v136, s41
	v_fma_f32 v137, |v133|, v137, s41
	v_fma_f32 v138, |v134|, v138, s41
	v_fma_f32 v139, |v135|, v139, s41
	v_fma_f32 v136, |v132|, v136, s42
; DI float bflo(unsigned u) { return __uint_as_float(u << 16); }
; DI float bfhi(unsigned u) { return __uint_as_float(u & 0xffff0000u); }
; DI void phase_peercoef(const Params& p, int bid, int nb) {
;     ...
;     for (int x = 0; x < 8; ++x) { const u32x2 pb = *(const u32x2*)(pd + (size_t)x * T_ * 128 + i4); d += (f32x4){bflo(pb[0]), bfhi(pb[0]), bflo(pb[1]), bfhi(pb[1])}; }
;     typedef int i32x4 __attribute__((ext_vector_type(4)));
;     const i32x4 e = *(const i32x4*)(eidx + i4); const f32x4 g = *(const f32x4*)(gate + i4);
;     ...
; #pragma unroll
;     for (int k = 0; k < 4; ++k) { const float dk = d[k] * uinv[e[k]]; o[k] = g[k] * 0.5f * dk * (1.f + erff(dk * 0.70710678118654752f)) * vinv[e[k]]; }
;     *(f32x4*)(coef + i4) = o;
	v_fma_f32 v137, |v133|, v137, s42
	v_fma_f32 v138, |v134|, v138, s42
	v_fma_f32 v139, |v135|, v139, s42
	v_fma_f32 v136, |v132|, v136, s43
	v_fma_f32 v137, |v133|, v137, s43
	v_fma_f32 v138, |v134|, v138, s43
	v_fma_f32 v139, |v135|, v139, s43
	v_fma_f32 v136, |v132|, v136, |v132|
	v_fma_f32 v137, |v133|, v137, |v133|
	v_fma_f32 v138, |v134|, v138, |v134|
	v_fma_f32 v139, |v135|, v139, |v135|
	v_mul_f32_e32 v140, 0xbfb8aa3b, v136
	v_mul_f32_e32 v141, 0xbfb8aa3b, v137
	v_mul_f32_e32 v142, 0xbfb8aa3b, v138
	v_mul_f32_e32 v143, 0xbfb8aa3b, v139
	v_fma_f32 v144, v136, s44, -v140
	v_fma_f32 v145, v137, s44, -v141
	v_fma_f32 v148, v138, s44, -v142
	v_fma_f32 v149, v139, s44, -v143
	v_rndne_f32_e32 v150, v140
	v_rndne_f32_e32 v151, v141
	v_rndne_f32_e32 v152, v142
	v_rndne_f32_e32 v153, v143
	v_fmac_f32_e32 v144, 0xb2a5705f, v136
	v_fmac_f32_e32 v145, 0xb2a5705f, v137
	v_fmac_f32_e32 v148, 0xb2a5705f, v138
	v_fmac_f32_e32 v149, 0xb2a5705f, v139
	v_sub_f32_e32 v140, v140, v150
	v_sub_f32_e32 v141, v141, v151
	v_sub_f32_e32 v142, v142, v152
	v_sub_f32_e32 v143, v143, v153
	v_add_f32_e32 v140, v140, v144
	v_add_f32_e32 v141, v141, v145
	v_add_f32_e32 v142, v142, v148
	v_add_f32_e32 v143, v143, v149
	v_cvt_i32_f32_e32 v150, v150
	v_cvt_i32_f32_e32 v151, v151
	v_cvt_i32_f32_e32 v152, v152
	v_cvt_i32_f32_e32 v153, v153
	v_exp_f32_e32 v140, v140
	v_exp_f32_e32 v141, v141
	v_exp_f32_e32 v142, v142
	v_exp_f32_e32 v143, v143
	v_cmp_nlt_f32_e64 vcc, s45, v136
	v_cmp_nlt_f32_e64 s[30:31], s45, v137
	v_cmp_nlt_f32_e64 s[34:35], s45, v138
	v_cmp_nlt_f32_e64 s[36:37], s45, v139
	v_ldexp_f32 v140, v140, v150
	v_ldexp_f32 v141, v141, v151
	v_ldexp_f32 v142, v142, v152
	v_ldexp_f32 v143, v143, v153
	v_cndmask_b32_e64 v140, 0, v140, vcc
	v_cndmask_b32_e64 v141, 0, v141, s[30:31]
	v_cndmask_b32_e64 v142, 0, v142, s[34:35]
	v_cndmask_b32_e64 v143, 0, v143, s[36:37]
	v_cmp_ngt_f32_e64 vcc, s46, v136
	v_cmp_ngt_f32_e64 s[30:31], s46, v137
	v_cmp_ngt_f32_e64 s[34:35], s46, v138
	v_cmp_ngt_f32_e64 s[36:37], s46, v139
	v_mul_f32_e32 v158, v132, v132
	v_mul_f32_e32 v159, v133, v133
	v_mul_f32_e32 v160, v134, v134
	v_mul_f32_e32 v161, v135, v135
	v_fmamk_f32 v154, v158, 0xba1345e1, v4
	v_fmamk_f32 v155, v159, 0xba1345e1, v4
	v_fmamk_f32 v156, v160, 0xba1345e1, v4
	v_fmamk_f32 v157, v161, 0xba1345e1, v4
	v_cndmask_b32_e64 v140, v6, v140, vcc
	v_cndmask_b32_e64 v141, v6, v141, s[30:31]
	v_cndmask_b32_e64 v142, v6, v142, s[34:35]
	v_cndmask_b32_e64 v143, v6, v143, s[36:37]
	v_sub_f32_e32 v162, 1.0, v140
	v_sub_f32_e32 v163, 1.0, v141
	v_sub_f32_e32 v164, 1.0, v142
	v_sub_f32_e32 v165, 1.0, v143
	v_fmaak_f32 v154, v158, v154, 0xbcdac9b8
	v_fmaak_f32 v155, v159, v155, 0xbcdac9b8
	v_fmaak_f32 v156, v160, v156, 0xbcdac9b8
	v_fmaak_f32 v157, v161, v157, 0xbcdac9b8
	v_fmaak_f32 v154, v158, v154, 0x3de703be
	v_fmaak_f32 v155, v159, v155, 0x3de703be
	v_fmaak_f32 v156, v160, v156, 0x3de703be
	v_fmaak_f32 v157, v161, v157, 0x3de703be
	v_fmaak_f32 v154, v158, v154, 0xbec09330
	v_fmaak_f32 v155, v159, v155, 0xbec09330
	v_fmaak_f32 v156, v160, v156, 0xbec09330
	v_fmaak_f32 v157, v161, v157, 0xbec09330
	v_fmaak_f32 v158, v158, v154, 0x3e0375d0
	v_fmaak_f32 v159, v159, v155, 0x3e0375d0
	v_fmaak_f32 v160, v160, v156, 0x3e0375d0
	v_fmaak_f32 v161, v161, v157, 0x3e0375d0
	v_fma_f32 v154, |v132|, v158, |v132|
	v_fma_f32 v155, |v133|, v159, |v133|
	v_fma_f32 v156, |v134|, v160, |v134|
	v_fma_f32 v157, |v135|, v161, |v135|
	v_cmp_nlt_f32_e64 vcc, |v132|, 1.0
	v_cmp_nlt_f32_e64 s[30:31], |v133|, 1.0
	v_cmp_nlt_f32_e64 s[34:35], |v134|, 1.0
	v_cmp_nlt_f32_e64 s[36:37], |v135|, 1.0
	v_mul_f32_e32 v166, 0.5, v60
	v_mul_f32_e32 v167, 0.5, v61
	v_mul_f32_e32 v168, 0.5, v62
	v_mul_f32_e32 v169, 0.5, v63
	v_mul_f32_e32 v166, v166, v128
	v_mul_f32_e32 v167, v167, v129
	v_mul_f32_e32 v168, v168, v130
	v_mul_f32_e32 v169, v169, v131
	v_cndmask_b32_e64 v162, v154, v162, vcc
	v_cndmask_b32_e64 v163, v155, v163, s[30:31]
	v_cndmask_b32_e64 v164, v156, v164, s[34:35]
	v_cndmask_b32_e64 v165, v157, v165, s[36:37]
	v_bfi_b32 v162, s47, v162, v132
	v_bfi_b32 v163, s47, v163, v133
	v_bfi_b32 v164, s47, v164, v134
	v_bfi_b32 v165, s47, v165, v135
	v_add_f32_e32 v162, 1.0, v162
	v_add_f32_e32 v163, 1.0, v163
	v_add_f32_e32 v164, 1.0, v164
	v_add_f32_e32 v165, 1.0, v165
	v_mul_f32_e32 v166, v166, v162
	v_mul_f32_e32 v167, v167, v163
	v_mul_f32_e32 v168, v168, v164
	v_mul_f32_e32 v169, v169, v165
	v_mul_f32_e32 v166, v100, v166
	v_mul_f32_e32 v167, v101, v167
	v_mul_f32_e32 v168, v102, v168
	v_mul_f32_e32 v169, v103, v169
	global_store_dwordx4 v108, v[166:169], s[26:27]
	v_add_u32_e32 v105, 0x400000, v10
	v_add_u32_e32 v108, 0x800000, v11
	global_load_dwordx4 v[56:59], v108, s[22:23]
	global_load_dwordx2 v[40:41], v105, s[0:1]
	global_load_dwordx2 v[42:43], v105, s[2:3]
	global_load_dwordx2 v[44:45], v105, s[4:5]
	global_load_dwordx2 v[46:47], v105, s[6:7]
	global_load_dwordx2 v[48:49], v105, s[8:9]
	global_load_dwordx2 v[50:51], v105, s[10:11]
	global_load_dwordx2 v[52:53], v105, s[12:13]
	global_load_dwordx2 v[54:55], v105, s[14:15]
	global_load_dwordx4 v[60:63], v108, s[24:25]
	s_waitcnt vmcnt(19)
	v_lshlrev_b32_e32 v112, 2, v32
	v_lshlrev_b32_e32 v113, 2, v33
	v_lshlrev_b32_e32 v114, 2, v34
	v_lshlrev_b32_e32 v115, 2, v35
	global_load_dword v96, v112, s[28:29]
	global_load_dword v97, v113, s[28:29]
	global_load_dword v98, v114, s[28:29]
	global_load_dword v99, v115, s[28:29]
	v_add_u32_e32 v116, 0x10000, v112
	v_add_u32_e32 v117, 0x10000, v113
	v_add_u32_e32 v118, 0x10000, v114
	v_add_u32_e32 v119, 0x10000, v115
	global_load_dword v100, v116, s[28:29]
	global_load_dword v101, v117, s[28:29]
	global_load_dword v102, v118, s[28:29]
	global_load_dword v103, v119, s[28:29]
	s_waitcnt vmcnt(19)
; DI float bflo(unsigned u) { return __uint_as_float(u << 16); }
; DI float bfhi(unsigned u) { return __uint_as_float(u & 0xffff0000u); }
; DI void phase_peercoef(const Params& p, int bid, int nb) {
;     ...
;     for (int x = 0; x < 8; ++x) { const u32x2 pb = *(const u32x2*)(pd + (size_t)x * T_ * 128 + i4); d += (f32x4){bflo(pb[0]), bfhi(pb[0]), bflo(pb[1]), bfhi(pb[1])}; }
;     typedef int i32x4 __attribute__((ext_vector_type(4)));
;     const i32x4 e = *(const i32x4*)(eidx + i4); const f32x4 g = *(const f32x4*)(gate + i4);
;     f32x4 o;
; #pragma unroll
;     for (int k = 0; k < 4; ++k) { const float dk = d[k] * uinv[e[k]]; o[k] = g[k] * 0.5f * dk * (1.f + erff(dk * 0.70710678118654752f)) * vinv[e[k]]; }
	v_lshlrev_b32_e32 v124, 16, v64
	v_and_b32_e32 v125, 0xffff0000, v64
	v_pk_add_f32 v[120:121], v[124:125], 0 op_sel_hi:[1,0]
	v_lshlrev_b32_e32 v124, 16, v66
	v_and_b32_e32 v125, 0xffff0000, v66
	v_pk_add_f32 v[120:121], v[120:121], v[124:125]
	v_lshlrev_b32_e32 v124, 16, v68
	v_and_b32_e32 v125, 0xffff0000, v68
	v_pk_add_f32 v[120:121], v[120:121], v[124:125]
	v_lshlrev_b32_e32 v124, 16, v70
	v_and_b32_e32 v125, 0xffff0000, v70
	v_pk_add_f32 v[120:121], v[120:121], v[124:125]
	v_lshlrev_b32_e32 v124, 16, v72
	v_and_b32_e32 v125, 0xffff0000, v72
	v_pk_add_f32 v[120:121], v[120:121], v[124:125]
	v_lshlrev_b32_e32 v124, 16, v74
	v_and_b32_e32 v125, 0xffff0000, v74
	v_pk_add_f32 v[120:121], v[120:121], v[124:125]
	v_lshlrev_b32_e32 v124, 16, v76
	v_and_b32_e32 v125, 0xffff0000, v76
	v_pk_add_f32 v[120:121], v[120:121], v[124:125]
	v_lshlrev_b32_e32 v124, 16, v78
	v_and_b32_e32 v125, 0xffff0000, v78
	v_pk_add_f32 v[120:121], v[120:121], v[124:125]
	v_lshlrev_b32_e32 v124, 16, v65
	v_and_b32_e32 v125, 0xffff0000, v65
	v_pk_add_f32 v[122:123], v[124:125], 0 op_sel_hi:[1,0]
	v_lshlrev_b32_e32 v124, 16, v67
	v_and_b32_e32 v125, 0xffff0000, v67
	v_pk_add_f32 v[122:123], v[122:123], v[124:125]
	v_lshlrev_b32_e32 v124, 16, v69
	v_and_b32_e32 v125, 0xffff0000, v69
	v_pk_add_f32 v[122:123], v[122:123], v[124:125]
	v_lshlrev_b32_e32 v124, 16, v71
	v_and_b32_e32 v125, 0xffff0000, v71
	v_pk_add_f32 v[122:123], v[122:123], v[124:125]
	v_lshlrev_b32_e32 v124, 16, v73
	v_and_b32_e32 v125, 0xffff0000, v73
	v_pk_add_f32 v[122:123], v[122:123], v[124:125]
	v_lshlrev_b32_e32 v124, 16, v75
	v_and_b32_e32 v125, 0xffff0000, v75
	v_pk_add_f32 v[122:123], v[122:123], v[124:125]
	v_lshlrev_b32_e32 v124, 16, v77
	v_and_b32_e32 v125, 0xffff0000, v77
	v_pk_add_f32 v[122:123], v[122:123], v[124:125]
	v_lshlrev_b32_e32 v124, 16, v79
	v_and_b32_e32 v125, 0xffff0000, v79
	v_pk_add_f32 v[122:123], v[122:123], v[124:125]
	v_mul_f32_e32 v128, v88, v120
	v_mul_f32_e32 v129, v89, v121
	v_mul_f32_e32 v130, v90, v122
	v_mul_f32_e32 v131, v91, v123
	v_mul_f32_e32 v132, 0x3f3504f3, v128
	v_mul_f32_e32 v133, 0x3f3504f3, v129
	v_mul_f32_e32 v134, 0x3f3504f3, v130
	v_mul_f32_e32 v135, 0x3f3504f3, v131
	v_fma_f32 v136, |v132|, s38, v5
	v_fma_f32 v137, |v133|, s38, v5
	v_fma_f32 v138, |v134|, s38, v5
	v_fma_f32 v139, |v135|, s38, v5
	v_fma_f32 v136, |v132|, v136, s39
	v_fma_f32 v137, |v133|, v137, s39
	v_fma_f32 v138, |v134|, v138, s39
	v_fma_f32 v139, |v135|, v139, s39
	v_fma_f32 v136, |v132|, v136, s40
	v_fma_f32 v137, |v133|, v137, s40
	v_fma_f32 v138, |v134|, v138, s40
	v_fma_f32 v139, |v135|, v139, s40
	v_fma_f32 v136, |v132|, v136, s41
	v_fma_f32 v137, |v133|, v137, s41
	v_fma_f32 v138, |v134|, v138, s41
	v_fma_f32 v139, |v135|, v139, s41
	v_fma_f32 v136, |v132|, v136, s42
	v_fma_f32 v137, |v133|, v137, s42
	v_fma_f32 v138, |v134|, v138, s42
	v_fma_f32 v139, |v135|, v139, s42
	v_fma_f32 v136, |v132|, v136, s43
	v_fma_f32 v137, |v133|, v137, s43
	v_fma_f32 v138, |v134|, v138, s43
	v_fma_f32 v139, |v135|, v139, s43
	v_fma_f32 v136, |v132|, v136, |v132|
	v_fma_f32 v137, |v133|, v137, |v133|
	v_fma_f32 v138, |v134|, v138, |v134|
	v_fma_f32 v139, |v135|, v139, |v135|
	v_mul_f32_e32 v140, 0xbfb8aa3b, v136
	v_mul_f32_e32 v141, 0xbfb8aa3b, v137
	v_mul_f32_e32 v142, 0xbfb8aa3b, v138
	v_mul_f32_e32 v143, 0xbfb8aa3b, v139
	v_fma_f32 v144, v136, s44, -v140
	v_fma_f32 v145, v137, s44, -v141
	v_fma_f32 v148, v138, s44, -v142
	v_fma_f32 v149, v139, s44, -v143
	v_rndne_f32_e32 v150, v140
	v_rndne_f32_e32 v151, v141
	v_rndne_f32_e32 v152, v142
	v_rndne_f32_e32 v153, v143
	v_fmac_f32_e32 v144, 0xb2a5705f, v136
	v_fmac_f32_e32 v145, 0xb2a5705f, v137
	v_fmac_f32_e32 v148, 0xb2a5705f, v138
	v_fmac_f32_e32 v149, 0xb2a5705f, v139
	v_sub_f32_e32 v140, v140, v150
	v_sub_f32_e32 v141, v141, v151
	v_sub_f32_e32 v142, v142, v152
	v_sub_f32_e32 v143, v143, v153
	v_add_f32_e32 v140, v140, v144
	v_add_f32_e32 v141, v141, v145
	v_add_f32_e32 v142, v142, v148
	v_add_f32_e32 v143, v143, v149
	v_cvt_i32_f32_e32 v150, v150
	v_cvt_i32_f32_e32 v151, v151
	v_cvt_i32_f32_e32 v152, v152
	v_cvt_i32_f32_e32 v153, v153
	v_exp_f32_e32 v140, v140
	v_exp_f32_e32 v141, v141
	v_exp_f32_e32 v142, v142
	v_exp_f32_e32 v143, v143
	v_cmp_nlt_f32_e64 vcc, s45, v136
	v_cmp_nlt_f32_e64 s[30:31], s45, v137
	v_cmp_nlt_f32_e64 s[34:35], s45, v138
	v_cmp_nlt_f32_e64 s[36:37], s45, v139
	v_ldexp_f32 v140, v140, v150
	v_ldexp_f32 v141, v141, v151
	v_ldexp_f32 v142, v142, v152
	v_ldexp_f32 v143, v143, v153
	v_cndmask_b32_e64 v140, 0, v140, vcc
	v_cndmask_b32_e64 v141, 0, v141, s[30:31]
	v_cndmask_b32_e64 v142, 0, v142, s[34:35]
	v_cndmask_b32_e64 v143, 0, v143, s[36:37]
	v_cmp_ngt_f32_e64 vcc, s46, v136
	v_cmp_ngt_f32_e64 s[30:31], s46, v137
	v_cmp_ngt_f32_e64 s[34:35], s46, v138
	v_cmp_ngt_f32_e64 s[36:37], s46, v139
	v_mul_f32_e32 v158, v132, v132
	v_mul_f32_e32 v159, v133, v133
	v_mul_f32_e32 v160, v134, v134
	v_mul_f32_e32 v161, v135, v135
	v_fmamk_f32 v154, v158, 0xba1345e1, v4
	v_fmamk_f32 v155, v159, 0xba1345e1, v4
	v_fmamk_f32 v156, v160, 0xba1345e1, v4
	v_fmamk_f32 v157, v161, 0xba1345e1, v4
	v_cndmask_b32_e64 v140, v6, v140, vcc
	v_cndmask_b32_e64 v141, v6, v141, s[30:31]
	v_cndmask_b32_e64 v142, v6, v142, s[34:35]
	v_cndmask_b32_e64 v143, v6, v143, s[36:37]
	v_sub_f32_e32 v162, 1.0, v140
	v_sub_f32_e32 v163, 1.0, v141
	v_sub_f32_e32 v164, 1.0, v142
	v_sub_f32_e32 v165, 1.0, v143
	v_fmaak_f32 v154, v158, v154, 0xbcdac9b8
	v_fmaak_f32 v155, v159, v155, 0xbcdac9b8
	v_fmaak_f32 v156, v160, v156, 0xbcdac9b8
	v_fmaak_f32 v157, v161, v157, 0xbcdac9b8
	v_fmaak_f32 v154, v158, v154, 0x3de703be
	v_fmaak_f32 v155, v159, v155, 0x3de703be
; DI float bflo(unsigned u) { return __uint_as_float(u << 16); }
; DI float bfhi(unsigned u) { return __uint_as_float(u & 0xffff0000u); }
; DI void phase_peercoef(const Params& p, int bid, int nb) {
;     ...
;     for (int x = 0; x < 8; ++x) { const u32x2 pb = *(const u32x2*)(pd + (size_t)x * T_ * 128 + i4); d += (f32x4){bflo(pb[0]), bfhi(pb[0]), bflo(pb[1]), bfhi(pb[1])}; }
;     typedef int i32x4 __attribute__((ext_vector_type(4)));
;     const i32x4 e = *(const i32x4*)(eidx + i4); const f32x4 g = *(const f32x4*)(gate + i4);
;     f32x4 o;
; #pragma unroll
;     for (int k = 0; k < 4; ++k) { const float dk = d[k] * uinv[e[k]]; o[k] = g[k] * 0.5f * dk * (1.f + erff(dk * 0.70710678118654752f)) * vinv[e[k]]; }
;     *(f32x4*)(coef + i4) = o;
	v_fmaak_f32 v156, v160, v156, 0x3de703be
	v_fmaak_f32 v157, v161, v157, 0x3de703be
	v_fmaak_f32 v154, v158, v154, 0xbec09330
	v_fmaak_f32 v155, v159, v155, 0xbec09330
	v_fmaak_f32 v156, v160, v156, 0xbec09330
	v_fmaak_f32 v157, v161, v157, 0xbec09330
	v_fmaak_f32 v158, v158, v154, 0x3e0375d0
	v_fmaak_f32 v159, v159, v155, 0x3e0375d0
	v_fmaak_f32 v160, v160, v156, 0x3e0375d0
	v_fmaak_f32 v161, v161, v157, 0x3e0375d0
	v_fma_f32 v154, |v132|, v158, |v132|
	v_fma_f32 v155, |v133|, v159, |v133|
	v_fma_f32 v156, |v134|, v160, |v134|
	v_fma_f32 v157, |v135|, v161, |v135|
	v_cmp_nlt_f32_e64 vcc, |v132|, 1.0
	v_cmp_nlt_f32_e64 s[30:31], |v133|, 1.0
	v_cmp_nlt_f32_e64 s[34:35], |v134|, 1.0
	v_cmp_nlt_f32_e64 s[36:37], |v135|, 1.0
	v_mul_f32_e32 v166, 0.5, v84
	v_mul_f32_e32 v167, 0.5, v85
	v_mul_f32_e32 v168, 0.5, v86
	v_mul_f32_e32 v169, 0.5, v87
	v_mul_f32_e32 v166, v166, v128
	v_mul_f32_e32 v167, v167, v129
	v_mul_f32_e32 v168, v168, v130
	v_mul_f32_e32 v169, v169, v131
	v_cndmask_b32_e64 v162, v154, v162, vcc
	v_cndmask_b32_e64 v163, v155, v163, s[30:31]
	v_cndmask_b32_e64 v164, v156, v164, s[34:35]
	v_cndmask_b32_e64 v165, v157, v165, s[36:37]
	v_bfi_b32 v162, s47, v162, v132
	v_bfi_b32 v163, s47, v163, v133
	v_bfi_b32 v164, s47, v164, v134
	v_bfi_b32 v165, s47, v165, v135
	v_add_f32_e32 v162, 1.0, v162
	v_add_f32_e32 v163, 1.0, v163
	v_add_f32_e32 v164, 1.0, v164
	v_add_f32_e32 v165, 1.0, v165
	v_mul_f32_e32 v166, v166, v162
	v_mul_f32_e32 v167, v167, v163
	v_mul_f32_e32 v168, v168, v164
	v_mul_f32_e32 v169, v169, v165
	v_mul_f32_e32 v166, v92, v166
	v_mul_f32_e32 v167, v93, v167
	v_mul_f32_e32 v168, v94, v168
	v_mul_f32_e32 v169, v95, v169
	global_store_dwordx4 v109, v[166:169], s[26:27]
	v_add_u32_e32 v106, 0x500000, v10
	v_add_u32_e32 v109, 0xa00000, v11
	global_load_dwordx4 v[80:83], v109, s[22:23]
	global_load_dwordx2 v[64:65], v106, s[0:1]
	global_load_dwordx2 v[66:67], v106, s[2:3]
	global_load_dwordx2 v[68:69], v106, s[4:5]
	global_load_dwordx2 v[70:71], v106, s[6:7]
	global_load_dwordx2 v[72:73], v106, s[8:9]
	global_load_dwordx2 v[74:75], v106, s[10:11]
	global_load_dwordx2 v[76:77], v106, s[12:13]
	global_load_dwordx2 v[78:79], v106, s[14:15]
	global_load_dwordx4 v[84:87], v109, s[24:25]
	s_waitcnt vmcnt(19)
	v_lshlrev_b32_e32 v112, 2, v56
	v_lshlrev_b32_e32 v113, 2, v57
	v_lshlrev_b32_e32 v114, 2, v58
	v_lshlrev_b32_e32 v115, 2, v59
	global_load_dword v88, v112, s[28:29]
	global_load_dword v89, v113, s[28:29]
	global_load_dword v90, v114, s[28:29]
	global_load_dword v91, v115, s[28:29]
	v_add_u32_e32 v116, 0x10000, v112
	v_add_u32_e32 v117, 0x10000, v113
	v_add_u32_e32 v118, 0x10000, v114
	v_add_u32_e32 v119, 0x10000, v115
	global_load_dword v92, v116, s[28:29]
	global_load_dword v93, v117, s[28:29]
	global_load_dword v94, v118, s[28:29]
	global_load_dword v95, v119, s[28:29]
	s_waitcnt vmcnt(19)
	v_lshlrev_b32_e32 v124, 16, v16
	v_and_b32_e32 v125, 0xffff0000, v16
	v_pk_add_f32 v[120:121], v[124:125], 0 op_sel_hi:[1,0]
	v_lshlrev_b32_e32 v124, 16, v18
	v_and_b32_e32 v125, 0xffff0000, v18
	v_pk_add_f32 v[120:121], v[120:121], v[124:125]
	v_lshlrev_b32_e32 v124, 16, v20
	v_and_b32_e32 v125, 0xffff0000, v20
	v_pk_add_f32 v[120:121], v[120:121], v[124:125]
	v_lshlrev_b32_e32 v124, 16, v22
	v_and_b32_e32 v125, 0xffff0000, v22
	v_pk_add_f32 v[120:121], v[120:121], v[124:125]
	v_lshlrev_b32_e32 v124, 16, v24
	v_and_b32_e32 v125, 0xffff0000, v24
	v_pk_add_f32 v[120:121], v[120:121], v[124:125]
	v_lshlrev_b32_e32 v124, 16, v26
	v_and_b32_e32 v125, 0xffff0000, v26
	v_pk_add_f32 v[120:121], v[120:121], v[124:125]
	v_lshlrev_b32_e32 v124, 16, v28
	v_and_b32_e32 v125, 0xffff0000, v28
	v_pk_add_f32 v[120:121], v[120:121], v[124:125]
	v_lshlrev_b32_e32 v124, 16, v30
	v_and_b32_e32 v125, 0xffff0000, v30
	v_pk_add_f32 v[120:121], v[120:121], v[124:125]
	v_lshlrev_b32_e32 v124, 16, v17
	v_and_b32_e32 v125, 0xffff0000, v17
	v_pk_add_f32 v[122:123], v[124:125], 0 op_sel_hi:[1,0]
	v_lshlrev_b32_e32 v124, 16, v19
	v_and_b32_e32 v125, 0xffff0000, v19
	v_pk_add_f32 v[122:123], v[122:123], v[124:125]
	v_lshlrev_b32_e32 v124, 16, v21
	v_and_b32_e32 v125, 0xffff0000, v21
	v_pk_add_f32 v[122:123], v[122:123], v[124:125]
	v_lshlrev_b32_e32 v124, 16, v23
	v_and_b32_e32 v125, 0xffff0000, v23
	v_pk_add_f32 v[122:123], v[122:123], v[124:125]
	v_lshlrev_b32_e32 v124, 16, v25
	v_and_b32_e32 v125, 0xffff0000, v25
	v_pk_add_f32 v[122:123], v[122:123], v[124:125]
	v_lshlrev_b32_e32 v124, 16, v27
	v_and_b32_e32 v125, 0xffff0000, v27
	v_pk_add_f32 v[122:123], v[122:123], v[124:125]
	v_lshlrev_b32_e32 v124, 16, v29
	v_and_b32_e32 v125, 0xffff0000, v29
	v_pk_add_f32 v[122:123], v[122:123], v[124:125]
	v_lshlrev_b32_e32 v124, 16, v31
	v_and_b32_e32 v125, 0xffff0000, v31
	v_pk_add_f32 v[122:123], v[122:123], v[124:125]
	v_mul_f32_e32 v128, v96, v120
	v_mul_f32_e32 v129, v97, v121
	v_mul_f32_e32 v130, v98, v122
	v_mul_f32_e32 v131, v99, v123
	v_mul_f32_e32 v132, 0x3f3504f3, v128
	v_mul_f32_e32 v133, 0x3f3504f3, v129
	v_mul_f32_e32 v134, 0x3f3504f3, v130
	v_mul_f32_e32 v135, 0x3f3504f3, v131
	v_fma_f32 v136, |v132|, s38, v5
	v_fma_f32 v137, |v133|, s38, v5
	v_fma_f32 v138, |v134|, s38, v5
	v_fma_f32 v139, |v135|, s38, v5
	v_fma_f32 v136, |v132|, v136, s39
	v_fma_f32 v137, |v133|, v137, s39
	v_fma_f32 v138, |v134|, v138, s39
	v_fma_f32 v139, |v135|, v139, s39
	v_fma_f32 v136, |v132|, v136, s40
	v_fma_f32 v137, |v133|, v137, s40
	v_fma_f32 v138, |v134|, v138, s40
	v_fma_f32 v139, |v135|, v139, s40
	v_fma_f32 v136, |v132|, v136, s41
	v_fma_f32 v137, |v133|, v137, s41
	v_fma_f32 v138, |v134|, v138, s41
	v_fma_f32 v139, |v135|, v139, s41
	v_fma_f32 v136, |v132|, v136, s42
; DI float bflo(unsigned u) { return __uint_as_float(u << 16); }
; DI float bfhi(unsigned u) { return __uint_as_float(u & 0xffff0000u); }
; DI void phase_peercoef(const Params& p, int bid, int nb) {
;     ...
;     for (int x = 0; x < 8; ++x) { const u32x2 pb = *(const u32x2*)(pd + (size_t)x * T_ * 128 + i4); d += (f32x4){bflo(pb[0]), bfhi(pb[0]), bflo(pb[1]), bfhi(pb[1])}; }
;     typedef int i32x4 __attribute__((ext_vector_type(4)));
;     const i32x4 e = *(const i32x4*)(eidx + i4); const f32x4 g = *(const f32x4*)(gate + i4);
;     ...
; #pragma unroll
;     for (int k = 0; k < 4; ++k) { const float dk = d[k] * uinv[e[k]]; o[k] = g[k] * 0.5f * dk * (1.f + erff(dk * 0.70710678118654752f)) * vinv[e[k]]; }
;     *(f32x4*)(coef + i4) = o;
	v_fma_f32 v137, |v133|, v137, s42
	v_fma_f32 v138, |v134|, v138, s42
	v_fma_f32 v139, |v135|, v139, s42
	v_fma_f32 v136, |v132|, v136, s43
	v_fma_f32 v137, |v133|, v137, s43
	v_fma_f32 v138, |v134|, v138, s43
	v_fma_f32 v139, |v135|, v139, s43
	v_fma_f32 v136, |v132|, v136, |v132|
	v_fma_f32 v137, |v133|, v137, |v133|
	v_fma_f32 v138, |v134|, v138, |v134|
	v_fma_f32 v139, |v135|, v139, |v135|
	v_mul_f32_e32 v140, 0xbfb8aa3b, v136
	v_mul_f32_e32 v141, 0xbfb8aa3b, v137
	v_mul_f32_e32 v142, 0xbfb8aa3b, v138
	v_mul_f32_e32 v143, 0xbfb8aa3b, v139
	v_fma_f32 v144, v136, s44, -v140
	v_fma_f32 v145, v137, s44, -v141
	v_fma_f32 v148, v138, s44, -v142
	v_fma_f32 v149, v139, s44, -v143
	v_rndne_f32_e32 v150, v140
	v_rndne_f32_e32 v151, v141
	v_rndne_f32_e32 v152, v142
	v_rndne_f32_e32 v153, v143
	v_fmac_f32_e32 v144, 0xb2a5705f, v136
	v_fmac_f32_e32 v145, 0xb2a5705f, v137
	v_fmac_f32_e32 v148, 0xb2a5705f, v138
	v_fmac_f32_e32 v149, 0xb2a5705f, v139
	v_sub_f32_e32 v140, v140, v150
	v_sub_f32_e32 v141, v141, v151
	v_sub_f32_e32 v142, v142, v152
	v_sub_f32_e32 v143, v143, v153
	v_add_f32_e32 v140, v140, v144
	v_add_f32_e32 v141, v141, v145
	v_add_f32_e32 v142, v142, v148
	v_add_f32_e32 v143, v143, v149
	v_cvt_i32_f32_e32 v150, v150
	v_cvt_i32_f32_e32 v151, v151
	v_cvt_i32_f32_e32 v152, v152
	v_cvt_i32_f32_e32 v153, v153
	v_exp_f32_e32 v140, v140
	v_exp_f32_e32 v141, v141
	v_exp_f32_e32 v142, v142
	v_exp_f32_e32 v143, v143
	v_cmp_nlt_f32_e64 vcc, s45, v136
	v_cmp_nlt_f32_e64 s[30:31], s45, v137
	v_cmp_nlt_f32_e64 s[34:35], s45, v138
	v_cmp_nlt_f32_e64 s[36:37], s45, v139
	v_ldexp_f32 v140, v140, v150
	v_ldexp_f32 v141, v141, v151
	v_ldexp_f32 v142, v142, v152
	v_ldexp_f32 v143, v143, v153
	v_cndmask_b32_e64 v140, 0, v140, vcc
	v_cndmask_b32_e64 v141, 0, v141, s[30:31]
	v_cndmask_b32_e64 v142, 0, v142, s[34:35]
	v_cndmask_b32_e64 v143, 0, v143, s[36:37]
	v_cmp_ngt_f32_e64 vcc, s46, v136
	v_cmp_ngt_f32_e64 s[30:31], s46, v137
	v_cmp_ngt_f32_e64 s[34:35], s46, v138
	v_cmp_ngt_f32_e64 s[36:37], s46, v139
	v_mul_f32_e32 v158, v132, v132
	v_mul_f32_e32 v159, v133, v133
	v_mul_f32_e32 v160, v134, v134
	v_mul_f32_e32 v161, v135, v135
	v_fmamk_f32 v154, v158, 0xba1345e1, v4
	v_fmamk_f32 v155, v159, 0xba1345e1, v4
	v_fmamk_f32 v156, v160, 0xba1345e1, v4
	v_fmamk_f32 v157, v161, 0xba1345e1, v4
	v_cndmask_b32_e64 v140, v6, v140, vcc
	v_cndmask_b32_e64 v141, v6, v141, s[30:31]
	v_cndmask_b32_e64 v142, v6, v142, s[34:35]
	v_cndmask_b32_e64 v143, v6, v143, s[36:37]
	v_sub_f32_e32 v162, 1.0, v140
	v_sub_f32_e32 v163, 1.0, v141
	v_sub_f32_e32 v164, 1.0, v142
	v_sub_f32_e32 v165, 1.0, v143
	v_fmaak_f32 v154, v158, v154, 0xbcdac9b8
	v_fmaak_f32 v155, v159, v155, 0xbcdac9b8
	v_fmaak_f32 v156, v160, v156, 0xbcdac9b8
	v_fmaak_f32 v157, v161, v157, 0xbcdac9b8
	v_fmaak_f32 v154, v158, v154, 0x3de703be
	v_fmaak_f32 v155, v159, v155, 0x3de703be
	v_fmaak_f32 v156, v160, v156, 0x3de703be
	v_fmaak_f32 v157, v161, v157, 0x3de703be
	v_fmaak_f32 v154, v158, v154, 0xbec09330
	v_fmaak_f32 v155, v159, v155, 0xbec09330
	v_fmaak_f32 v156, v160, v156, 0xbec09330
	v_fmaak_f32 v157, v161, v157, 0xbec09330
	v_fmaak_f32 v158, v158, v154, 0x3e0375d0
	v_fmaak_f32 v159, v159, v155, 0x3e0375d0
	v_fmaak_f32 v160, v160, v156, 0x3e0375d0
	v_fmaak_f32 v161, v161, v157, 0x3e0375d0
	v_fma_f32 v154, |v132|, v158, |v132|
	v_fma_f32 v155, |v133|, v159, |v133|
	v_fma_f32 v156, |v134|, v160, |v134|
	v_fma_f32 v157, |v135|, v161, |v135|
	v_cmp_nlt_f32_e64 vcc, |v132|, 1.0
	v_cmp_nlt_f32_e64 s[30:31], |v133|, 1.0
	v_cmp_nlt_f32_e64 s[34:35], |v134|, 1.0
	v_cmp_nlt_f32_e64 s[36:37], |v135|, 1.0
	v_mul_f32_e32 v166, 0.5, v36
	v_mul_f32_e32 v167, 0.5, v37
	v_mul_f32_e32 v168, 0.5, v38
	v_mul_f32_e32 v169, 0.5, v39
	v_mul_f32_e32 v166, v166, v128
	v_mul_f32_e32 v167, v167, v129
	v_mul_f32_e32 v168, v168, v130
	v_mul_f32_e32 v169, v169, v131
	v_cndmask_b32_e64 v162, v154, v162, vcc
	v_cndmask_b32_e64 v163, v155, v163, s[30:31]
	v_cndmask_b32_e64 v164, v156, v164, s[34:35]
	v_cndmask_b32_e64 v165, v157, v165, s[36:37]
	v_bfi_b32 v162, s47, v162, v132
	v_bfi_b32 v163, s47, v163, v133
	v_bfi_b32 v164, s47, v164, v134
	v_bfi_b32 v165, s47, v165, v135
	v_add_f32_e32 v162, 1.0, v162
	v_add_f32_e32 v163, 1.0, v163
	v_add_f32_e32 v164, 1.0, v164
	v_add_f32_e32 v165, 1.0, v165
	v_mul_f32_e32 v166, v166, v162
	v_mul_f32_e32 v167, v167, v163
	v_mul_f32_e32 v168, v168, v164
	v_mul_f32_e32 v169, v169, v165
	v_mul_f32_e32 v166, v100, v166
	v_mul_f32_e32 v167, v101, v167
	v_mul_f32_e32 v168, v102, v168
	v_mul_f32_e32 v169, v103, v169
	global_store_dwordx4 v107, v[166:169], s[26:27]
	v_add_u32_e32 v104, 0x600000, v10
	v_add_u32_e32 v107, 0xc00000, v11
	global_load_dwordx4 v[32:35], v107, s[22:23]
	global_load_dwordx2 v[16:17], v104, s[0:1]
	global_load_dwordx2 v[18:19], v104, s[2:3]
	global_load_dwordx2 v[20:21], v104, s[4:5]
	global_load_dwordx2 v[22:23], v104, s[6:7]
	global_load_dwordx2 v[24:25], v104, s[8:9]
	global_load_dwordx2 v[26:27], v104, s[10:11]
	global_load_dwordx2 v[28:29], v104, s[12:13]
	global_load_dwordx2 v[30:31], v104, s[14:15]
	global_load_dwordx4 v[36:39], v107, s[24:25]
	s_waitcnt vmcnt(19)
	v_lshlrev_b32_e32 v112, 2, v80
	v_lshlrev_b32_e32 v113, 2, v81
	v_lshlrev_b32_e32 v114, 2, v82
	v_lshlrev_b32_e32 v115, 2, v83
	global_load_dword v96, v112, s[28:29]
	global_load_dword v97, v113, s[28:29]
	global_load_dword v98, v114, s[28:29]
	global_load_dword v99, v115, s[28:29]
	v_add_u32_e32 v116, 0x10000, v112
	v_add_u32_e32 v117, 0x10000, v113
	v_add_u32_e32 v118, 0x10000, v114
	v_add_u32_e32 v119, 0x10000, v115
	global_load_dword v100, v116, s[28:29]
	global_load_dword v101, v117, s[28:29]
	global_load_dword v102, v118, s[28:29]
	global_load_dword v103, v119, s[28:29]
	s_waitcnt vmcnt(19)
; DI float bflo(unsigned u) { return __uint_as_float(u << 16); }
; DI float bfhi(unsigned u) { return __uint_as_float(u & 0xffff0000u); }
; DI void phase_peercoef(const Params& p, int bid, int nb) {
;     ...
;     for (int x = 0; x < 8; ++x) { const u32x2 pb = *(const u32x2*)(pd + (size_t)x * T_ * 128 + i4); d += (f32x4){bflo(pb[0]), bfhi(pb[0]), bflo(pb[1]), bfhi(pb[1])}; }
;     typedef int i32x4 __attribute__((ext_vector_type(4)));
;     const i32x4 e = *(const i32x4*)(eidx + i4); const f32x4 g = *(const f32x4*)(gate + i4);
;     f32x4 o;
; #pragma unroll
;     for (int k = 0; k < 4; ++k) { const float dk = d[k] * uinv[e[k]]; o[k] = g[k] * 0.5f * dk * (1.f + erff(dk * 0.70710678118654752f)) * vinv[e[k]]; }
	v_lshlrev_b32_e32 v124, 16, v40
	v_and_b32_e32 v125, 0xffff0000, v40
	v_pk_add_f32 v[120:121], v[124:125], 0 op_sel_hi:[1,0]
	v_lshlrev_b32_e32 v124, 16, v42
	v_and_b32_e32 v125, 0xffff0000, v42
	v_pk_add_f32 v[120:121], v[120:121], v[124:125]
	v_lshlrev_b32_e32 v124, 16, v44
	v_and_b32_e32 v125, 0xffff0000, v44
	v_pk_add_f32 v[120:121], v[120:121], v[124:125]
	v_lshlrev_b32_e32 v124, 16, v46
	v_and_b32_e32 v125, 0xffff0000, v46
	v_pk_add_f32 v[120:121], v[120:121], v[124:125]
	v_lshlrev_b32_e32 v124, 16, v48
	v_and_b32_e32 v125, 0xffff0000, v48
	v_pk_add_f32 v[120:121], v[120:121], v[124:125]
	v_lshlrev_b32_e32 v124, 16, v50
	v_and_b32_e32 v125, 0xffff0000, v50
	v_pk_add_f32 v[120:121], v[120:121], v[124:125]
	v_lshlrev_b32_e32 v124, 16, v52
	v_and_b32_e32 v125, 0xffff0000, v52
	v_pk_add_f32 v[120:121], v[120:121], v[124:125]
	v_lshlrev_b32_e32 v124, 16, v54
	v_and_b32_e32 v125, 0xffff0000, v54
	v_pk_add_f32 v[120:121], v[120:121], v[124:125]
	v_lshlrev_b32_e32 v124, 16, v41
	v_and_b32_e32 v125, 0xffff0000, v41
	v_pk_add_f32 v[122:123], v[124:125], 0 op_sel_hi:[1,0]
	v_lshlrev_b32_e32 v124, 16, v43
	v_and_b32_e32 v125, 0xffff0000, v43
	v_pk_add_f32 v[122:123], v[122:123], v[124:125]
	v_lshlrev_b32_e32 v124, 16, v45
	v_and_b32_e32 v125, 0xffff0000, v45
	v_pk_add_f32 v[122:123], v[122:123], v[124:125]
	v_lshlrev_b32_e32 v124, 16, v47
	v_and_b32_e32 v125, 0xffff0000, v47
	v_pk_add_f32 v[122:123], v[122:123], v[124:125]
	v_lshlrev_b32_e32 v124, 16, v49
	v_and_b32_e32 v125, 0xffff0000, v49
	v_pk_add_f32 v[122:123], v[122:123], v[124:125]
	v_lshlrev_b32_e32 v124, 16, v51
	v_and_b32_e32 v125, 0xffff0000, v51
	v_pk_add_f32 v[122:123], v[122:123], v[124:125]
	v_lshlrev_b32_e32 v124, 16, v53
	v_and_b32_e32 v125, 0xffff0000, v53
	v_pk_add_f32 v[122:123], v[122:123], v[124:125]
	v_lshlrev_b32_e32 v124, 16, v55
	v_and_b32_e32 v125, 0xffff0000, v55
	v_pk_add_f32 v[122:123], v[122:123], v[124:125]
	v_mul_f32_e32 v128, v88, v120
	v_mul_f32_e32 v129, v89, v121
	v_mul_f32_e32 v130, v90, v122
	v_mul_f32_e32 v131, v91, v123
	v_mul_f32_e32 v132, 0x3f3504f3, v128
	v_mul_f32_e32 v133, 0x3f3504f3, v129
	v_mul_f32_e32 v134, 0x3f3504f3, v130
	v_mul_f32_e32 v135, 0x3f3504f3, v131
	v_fma_f32 v136, |v132|, s38, v5
	v_fma_f32 v137, |v133|, s38, v5
	v_fma_f32 v138, |v134|, s38, v5
	v_fma_f32 v139, |v135|, s38, v5
	v_fma_f32 v136, |v132|, v136, s39
	v_fma_f32 v137, |v133|, v137, s39
	v_fma_f32 v138, |v134|, v138, s39
	v_fma_f32 v139, |v135|, v139, s39
	v_fma_f32 v136, |v132|, v136, s40
	v_fma_f32 v137, |v133|, v137, s40
	v_fma_f32 v138, |v134|, v138, s40
	v_fma_f32 v139, |v135|, v139, s40
	v_fma_f32 v136, |v132|, v136, s41
	v_fma_f32 v137, |v133|, v137, s41
	v_fma_f32 v138, |v134|, v138, s41
	v_fma_f32 v139, |v135|, v139, s41
	v_fma_f32 v136, |v132|, v136, s42
	v_fma_f32 v137, |v133|, v137, s42
	v_fma_f32 v138, |v134|, v138, s42
	v_fma_f32 v139, |v135|, v139, s42
	v_fma_f32 v136, |v132|, v136, s43
	v_fma_f32 v137, |v133|, v137, s43
	v_fma_f32 v138, |v134|, v138, s43
	v_fma_f32 v139, |v135|, v139, s43
	v_fma_f32 v136, |v132|, v136, |v132|
	v_fma_f32 v137, |v133|, v137, |v133|
	v_fma_f32 v138, |v134|, v138, |v134|
	v_fma_f32 v139, |v135|, v139, |v135|
	v_mul_f32_e32 v140, 0xbfb8aa3b, v136
	v_mul_f32_e32 v141, 0xbfb8aa3b, v137
	v_mul_f32_e32 v142, 0xbfb8aa3b, v138
	v_mul_f32_e32 v143, 0xbfb8aa3b, v139
	v_fma_f32 v144, v136, s44, -v140
	v_fma_f32 v145, v137, s44, -v141
	v_fma_f32 v148, v138, s44, -v142
	v_fma_f32 v149, v139, s44, -v143
	v_rndne_f32_e32 v150, v140
	v_rndne_f32_e32 v151, v141
	v_rndne_f32_e32 v152, v142
	v_rndne_f32_e32 v153, v143
	v_fmac_f32_e32 v144, 0xb2a5705f, v136
	v_fmac_f32_e32 v145, 0xb2a5705f, v137
	v_fmac_f32_e32 v148, 0xb2a5705f, v138
	v_fmac_f32_e32 v149, 0xb2a5705f, v139
	v_sub_f32_e32 v140, v140, v150
	v_sub_f32_e32 v141, v141, v151
	v_sub_f32_e32 v142, v142, v152
	v_sub_f32_e32 v143, v143, v153
	v_add_f32_e32 v140, v140, v144
	v_add_f32_e32 v141, v141, v145
	v_add_f32_e32 v142, v142, v148
	v_add_f32_e32 v143, v143, v149
	v_cvt_i32_f32_e32 v150, v150
	v_cvt_i32_f32_e32 v151, v151
	v_cvt_i32_f32_e32 v152, v152
	v_cvt_i32_f32_e32 v153, v153
	v_exp_f32_e32 v140, v140
	v_exp_f32_e32 v141, v141
	v_exp_f32_e32 v142, v142
	v_exp_f32_e32 v143, v143
	v_cmp_nlt_f32_e64 vcc, s45, v136
	v_cmp_nlt_f32_e64 s[30:31], s45, v137
	v_cmp_nlt_f32_e64 s[34:35], s45, v138
	v_cmp_nlt_f32_e64 s[36:37], s45, v139
	v_ldexp_f32 v140, v140, v150
	v_ldexp_f32 v141, v141, v151
	v_ldexp_f32 v142, v142, v152
	v_ldexp_f32 v143, v143, v153
	v_cndmask_b32_e64 v140, 0, v140, vcc
	v_cndmask_b32_e64 v141, 0, v141, s[30:31]
	v_cndmask_b32_e64 v142, 0, v142, s[34:35]
	v_cndmask_b32_e64 v143, 0, v143, s[36:37]
	v_cmp_ngt_f32_e64 vcc, s46, v136
	v_cmp_ngt_f32_e64 s[30:31], s46, v137
	v_cmp_ngt_f32_e64 s[34:35], s46, v138
	v_cmp_ngt_f32_e64 s[36:37], s46, v139
	v_mul_f32_e32 v158, v132, v132
	v_mul_f32_e32 v159, v133, v133
	v_mul_f32_e32 v160, v134, v134
	v_mul_f32_e32 v161, v135, v135
	v_fmamk_f32 v154, v158, 0xba1345e1, v4
	v_fmamk_f32 v155, v159, 0xba1345e1, v4
	v_fmamk_f32 v156, v160, 0xba1345e1, v4
	v_fmamk_f32 v157, v161, 0xba1345e1, v4
	v_cndmask_b32_e64 v140, v6, v140, vcc
	v_cndmask_b32_e64 v141, v6, v141, s[30:31]
	v_cndmask_b32_e64 v142, v6, v142, s[34:35]
	v_cndmask_b32_e64 v143, v6, v143, s[36:37]
	v_sub_f32_e32 v162, 1.0, v140
	v_sub_f32_e32 v163, 1.0, v141
	v_sub_f32_e32 v164, 1.0, v142
	v_sub_f32_e32 v165, 1.0, v143
	v_fmaak_f32 v154, v158, v154, 0xbcdac9b8
	v_fmaak_f32 v155, v159, v155, 0xbcdac9b8
	v_fmaak_f32 v156, v160, v156, 0xbcdac9b8
	v_fmaak_f32 v157, v161, v157, 0xbcdac9b8
	v_fmaak_f32 v154, v158, v154, 0x3de703be
	v_fmaak_f32 v155, v159, v155, 0x3de703be
; DI int tidx() { int t = threadIdx.x & 255; asm volatile("" : "+v"(t)); return t; }
; DI float bflo(unsigned u) { return __uint_as_float(u << 16); }
; DI float bfhi(unsigned u) { return __uint_as_float(u & 0xffff0000u); }
; DI void phase_peercoef(const Params& p, int bid, int nb) {
;     ...
;   for (size_t i4 = ((size_t)bid * NT + tidx()) * 4; i4 < (size_t)T_ * 128; i4 += (size_t)nb * NT * 4) {
;     f32x4 d = {0.f, 0.f, 0.f, 0.f};
; #pragma unroll
;     for (int x = 0; x < 8; ++x) { const u32x2 pb = *(const u32x2*)(pd + (size_t)x * T_ * 128 + i4); d += (f32x4){bflo(pb[0]), bfhi(pb[0]), bflo(pb[1]), bfhi(pb[1])}; }
;     typedef int i32x4 __attribute__((ext_vector_type(4)));
;     const i32x4 e = *(const i32x4*)(eidx + i4); const f32x4 g = *(const f32x4*)(gate + i4);
;     f32x4 o;
; #pragma unroll
;     for (int k = 0; k < 4; ++k) { const float dk = d[k] * uinv[e[k]]; o[k] = g[k] * 0.5f * dk * (1.f + erff(dk * 0.70710678118654752f)) * vinv[e[k]]; }
;     *(f32x4*)(coef + i4) = o;
	v_fmaak_f32 v156, v160, v156, 0x3de703be
	v_fmaak_f32 v157, v161, v157, 0x3de703be
	v_fmaak_f32 v154, v158, v154, 0xbec09330
	v_fmaak_f32 v155, v159, v155, 0xbec09330
	v_fmaak_f32 v156, v160, v156, 0xbec09330
	v_fmaak_f32 v157, v161, v157, 0xbec09330
	v_fmaak_f32 v158, v158, v154, 0x3e0375d0
	v_fmaak_f32 v159, v159, v155, 0x3e0375d0
	v_fmaak_f32 v160, v160, v156, 0x3e0375d0
	v_fmaak_f32 v161, v161, v157, 0x3e0375d0
	v_fma_f32 v154, |v132|, v158, |v132|
	v_fma_f32 v155, |v133|, v159, |v133|
	v_fma_f32 v156, |v134|, v160, |v134|
	v_fma_f32 v157, |v135|, v161, |v135|
	v_cmp_nlt_f32_e64 vcc, |v132|, 1.0
	v_cmp_nlt_f32_e64 s[30:31], |v133|, 1.0
	v_cmp_nlt_f32_e64 s[34:35], |v134|, 1.0
	v_cmp_nlt_f32_e64 s[36:37], |v135|, 1.0
	v_mul_f32_e32 v166, 0.5, v60
	v_mul_f32_e32 v167, 0.5, v61
	v_mul_f32_e32 v168, 0.5, v62
	v_mul_f32_e32 v169, 0.5, v63
	v_mul_f32_e32 v166, v166, v128
	v_mul_f32_e32 v167, v167, v129
	v_mul_f32_e32 v168, v168, v130
	v_mul_f32_e32 v169, v169, v131
	v_cndmask_b32_e64 v162, v154, v162, vcc
	v_cndmask_b32_e64 v163, v155, v163, s[30:31]
	v_cndmask_b32_e64 v164, v156, v164, s[34:35]
	v_cndmask_b32_e64 v165, v157, v165, s[36:37]
	v_bfi_b32 v162, s47, v162, v132
	v_bfi_b32 v163, s47, v163, v133
	v_bfi_b32 v164, s47, v164, v134
	v_bfi_b32 v165, s47, v165, v135
	v_add_f32_e32 v162, 1.0, v162
	v_add_f32_e32 v163, 1.0, v163
	v_add_f32_e32 v164, 1.0, v164
	v_add_f32_e32 v165, 1.0, v165
	v_mul_f32_e32 v166, v166, v162
	v_mul_f32_e32 v167, v167, v163
	v_mul_f32_e32 v168, v168, v164
	v_mul_f32_e32 v169, v169, v165
	v_mul_f32_e32 v166, v92, v166
	v_mul_f32_e32 v167, v93, v167
	v_mul_f32_e32 v168, v94, v168
	v_mul_f32_e32 v169, v95, v169
	global_store_dwordx4 v108, v[166:169], s[26:27]
	v_add_u32_e32 v105, 0x700000, v10
	v_add_u32_e32 v108, 0xe00000, v11
	global_load_dwordx4 v[56:59], v108, s[22:23]
	global_load_dwordx2 v[40:41], v105, s[0:1]
	global_load_dwordx2 v[42:43], v105, s[2:3]
	global_load_dwordx2 v[44:45], v105, s[4:5]
	global_load_dwordx2 v[46:47], v105, s[6:7]
	global_load_dwordx2 v[48:49], v105, s[8:9]
	global_load_dwordx2 v[50:51], v105, s[10:11]
	global_load_dwordx2 v[52:53], v105, s[12:13]
	global_load_dwordx2 v[54:55], v105, s[14:15]
	global_load_dwordx4 v[60:63], v108, s[24:25]
	s_waitcnt vmcnt(19)
	v_lshlrev_b32_e32 v112, 2, v32
	v_lshlrev_b32_e32 v113, 2, v33
	v_lshlrev_b32_e32 v114, 2, v34
	v_lshlrev_b32_e32 v115, 2, v35
	global_load_dword v88, v112, s[28:29]
	global_load_dword v89, v113, s[28:29]
	global_load_dword v90, v114, s[28:29]
	global_load_dword v91, v115, s[28:29]
	v_add_u32_e32 v116, 0x10000, v112
	v_add_u32_e32 v117, 0x10000, v113
	v_add_u32_e32 v118, 0x10000, v114
	v_add_u32_e32 v119, 0x10000, v115
	global_load_dword v92, v116, s[28:29]
	global_load_dword v93, v117, s[28:29]
	global_load_dword v94, v118, s[28:29]
	global_load_dword v95, v119, s[28:29]
	s_waitcnt vmcnt(19)
	v_lshlrev_b32_e32 v124, 16, v64
	v_and_b32_e32 v125, 0xffff0000, v64
	v_pk_add_f32 v[120:121], v[124:125], 0 op_sel_hi:[1,0]
	v_lshlrev_b32_e32 v124, 16, v66
	v_and_b32_e32 v125, 0xffff0000, v66
	v_pk_add_f32 v[120:121], v[120:121], v[124:125]
	v_lshlrev_b32_e32 v124, 16, v68
	v_and_b32_e32 v125, 0xffff0000, v68
	v_pk_add_f32 v[120:121], v[120:121], v[124:125]
	v_lshlrev_b32_e32 v124, 16, v70
	v_and_b32_e32 v125, 0xffff0000, v70
	v_pk_add_f32 v[120:121], v[120:121], v[124:125]
	v_lshlrev_b32_e32 v124, 16, v72
	v_and_b32_e32 v125, 0xffff0000, v72
	v_pk_add_f32 v[120:121], v[120:121], v[124:125]
	v_lshlrev_b32_e32 v124, 16, v74
	v_and_b32_e32 v125, 0xffff0000, v74
	v_pk_add_f32 v[120:121], v[120:121], v[124:125]
	v_lshlrev_b32_e32 v124, 16, v76
	v_and_b32_e32 v125, 0xffff0000, v76
	v_pk_add_f32 v[120:121], v[120:121], v[124:125]
	v_lshlrev_b32_e32 v124, 16, v78
	v_and_b32_e32 v125, 0xffff0000, v78
	v_pk_add_f32 v[120:121], v[120:121], v[124:125]
	v_lshlrev_b32_e32 v124, 16, v65
	v_and_b32_e32 v125, 0xffff0000, v65
	v_pk_add_f32 v[122:123], v[124:125], 0 op_sel_hi:[1,0]
	v_lshlrev_b32_e32 v124, 16, v67
	v_and_b32_e32 v125, 0xffff0000, v67
	v_pk_add_f32 v[122:123], v[122:123], v[124:125]
	v_lshlrev_b32_e32 v124, 16, v69
	v_and_b32_e32 v125, 0xffff0000, v69
	v_pk_add_f32 v[122:123], v[122:123], v[124:125]
	v_lshlrev_b32_e32 v124, 16, v71
	v_and_b32_e32 v125, 0xffff0000, v71
	v_pk_add_f32 v[122:123], v[122:123], v[124:125]
	v_lshlrev_b32_e32 v124, 16, v73
	v_and_b32_e32 v125, 0xffff0000, v73
	v_pk_add_f32 v[122:123], v[122:123], v[124:125]
	v_lshlrev_b32_e32 v124, 16, v75
	v_and_b32_e32 v125, 0xffff0000, v75
	v_pk_add_f32 v[122:123], v[122:123], v[124:125]
	v_lshlrev_b32_e32 v124, 16, v77
	v_and_b32_e32 v125, 0xffff0000, v77
	v_pk_add_f32 v[122:123], v[122:123], v[124:125]
	v_lshlrev_b32_e32 v124, 16, v79
	v_and_b32_e32 v125, 0xffff0000, v79
	v_pk_add_f32 v[122:123], v[122:123], v[124:125]
	v_mul_f32_e32 v128, v96, v120
	v_mul_f32_e32 v129, v97, v121
	v_mul_f32_e32 v130, v98, v122
	v_mul_f32_e32 v131, v99, v123
	v_mul_f32_e32 v132, 0x3f3504f3, v128
	v_mul_f32_e32 v133, 0x3f3504f3, v129
	v_mul_f32_e32 v134, 0x3f3504f3, v130
	v_mul_f32_e32 v135, 0x3f3504f3, v131
	v_fma_f32 v136, |v132|, s38, v5
	v_fma_f32 v137, |v133|, s38, v5
	v_fma_f32 v138, |v134|, s38, v5
	v_fma_f32 v139, |v135|, s38, v5
	v_fma_f32 v136, |v132|, v136, s39
	v_fma_f32 v137, |v133|, v137, s39
	v_fma_f32 v138, |v134|, v138, s39
	v_fma_f32 v139, |v135|, v139, s39
	v_fma_f32 v136, |v132|, v136, s40
	v_fma_f32 v137, |v133|, v137, s40
	v_fma_f32 v138, |v134|, v138, s40
	v_fma_f32 v139, |v135|, v139, s40
	v_fma_f32 v136, |v132|, v136, s41
	v_fma_f32 v137, |v133|, v137, s41
	v_fma_f32 v138, |v134|, v138, s41
	v_fma_f32 v139, |v135|, v139, s41
	v_fma_f32 v136, |v132|, v136, s42
; DI float bflo(unsigned u) { return __uint_as_float(u << 16); }
; DI float bfhi(unsigned u) { return __uint_as_float(u & 0xffff0000u); }
; DI void phase_peercoef(const Params& p, int bid, int nb) {
;     ...
;     for (int x = 0; x < 8; ++x) { const u32x2 pb = *(const u32x2*)(pd + (size_t)x * T_ * 128 + i4); d += (f32x4){bflo(pb[0]), bfhi(pb[0]), bflo(pb[1]), bfhi(pb[1])}; }
;     typedef int i32x4 __attribute__((ext_vector_type(4)));
;     const i32x4 e = *(const i32x4*)(eidx + i4); const f32x4 g = *(const f32x4*)(gate + i4);
;     ...
;     for (int k = 0; k < 4; ++k) { const float dk = d[k] * uinv[e[k]]; o[k] = g[k] * 0.5f * dk * (1.f + erff(dk * 0.70710678118654752f)) * vinv[e[k]]; }
;     *(f32x4*)(coef + i4) = o;
	v_fma_f32 v137, |v133|, v137, s42
	v_fma_f32 v138, |v134|, v138, s42
	v_fma_f32 v139, |v135|, v139, s42
	v_fma_f32 v136, |v132|, v136, s43
	v_fma_f32 v137, |v133|, v137, s43
	v_fma_f32 v138, |v134|, v138, s43
	v_fma_f32 v139, |v135|, v139, s43
	v_fma_f32 v136, |v132|, v136, |v132|
	v_fma_f32 v137, |v133|, v137, |v133|
	v_fma_f32 v138, |v134|, v138, |v134|
	v_fma_f32 v139, |v135|, v139, |v135|
	v_mul_f32_e32 v140, 0xbfb8aa3b, v136
	v_mul_f32_e32 v141, 0xbfb8aa3b, v137
	v_mul_f32_e32 v142, 0xbfb8aa3b, v138
	v_mul_f32_e32 v143, 0xbfb8aa3b, v139
	v_fma_f32 v144, v136, s44, -v140
	v_fma_f32 v145, v137, s44, -v141
	v_fma_f32 v148, v138, s44, -v142
	v_fma_f32 v149, v139, s44, -v143
	v_rndne_f32_e32 v150, v140
	v_rndne_f32_e32 v151, v141
	v_rndne_f32_e32 v152, v142
	v_rndne_f32_e32 v153, v143
	v_fmac_f32_e32 v144, 0xb2a5705f, v136
	v_fmac_f32_e32 v145, 0xb2a5705f, v137
	v_fmac_f32_e32 v148, 0xb2a5705f, v138
	v_fmac_f32_e32 v149, 0xb2a5705f, v139
	v_sub_f32_e32 v140, v140, v150
	v_sub_f32_e32 v141, v141, v151
	v_sub_f32_e32 v142, v142, v152
	v_sub_f32_e32 v143, v143, v153
	v_add_f32_e32 v140, v140, v144
	v_add_f32_e32 v141, v141, v145
	v_add_f32_e32 v142, v142, v148
	v_add_f32_e32 v143, v143, v149
	v_cvt_i32_f32_e32 v150, v150
	v_cvt_i32_f32_e32 v151, v151
	v_cvt_i32_f32_e32 v152, v152
	v_cvt_i32_f32_e32 v153, v153
	v_exp_f32_e32 v140, v140
	v_exp_f32_e32 v141, v141
	v_exp_f32_e32 v142, v142
	v_exp_f32_e32 v143, v143
	v_cmp_nlt_f32_e64 vcc, s45, v136
	v_cmp_nlt_f32_e64 s[30:31], s45, v137
	v_cmp_nlt_f32_e64 s[34:35], s45, v138
	v_cmp_nlt_f32_e64 s[36:37], s45, v139
	v_ldexp_f32 v140, v140, v150
	v_ldexp_f32 v141, v141, v151
	v_ldexp_f32 v142, v142, v152
	v_ldexp_f32 v143, v143, v153
	v_cndmask_b32_e64 v140, 0, v140, vcc
	v_cndmask_b32_e64 v141, 0, v141, s[30:31]
	v_cndmask_b32_e64 v142, 0, v142, s[34:35]
	v_cndmask_b32_e64 v143, 0, v143, s[36:37]
	v_cmp_ngt_f32_e64 vcc, s46, v136
	v_cmp_ngt_f32_e64 s[30:31], s46, v137
	v_cmp_ngt_f32_e64 s[34:35], s46, v138
	v_cmp_ngt_f32_e64 s[36:37], s46, v139
	v_mul_f32_e32 v158, v132, v132
	v_mul_f32_e32 v159, v133, v133
	v_mul_f32_e32 v160, v134, v134
	v_mul_f32_e32 v161, v135, v135
	v_fmamk_f32 v154, v158, 0xba1345e1, v4
	v_fmamk_f32 v155, v159, 0xba1345e1, v4
	v_fmamk_f32 v156, v160, 0xba1345e1, v4
	v_fmamk_f32 v157, v161, 0xba1345e1, v4
	v_cndmask_b32_e64 v140, v6, v140, vcc
	v_cndmask_b32_e64 v141, v6, v141, s[30:31]
	v_cndmask_b32_e64 v142, v6, v142, s[34:35]
	v_cndmask_b32_e64 v143, v6, v143, s[36:37]
	v_sub_f32_e32 v162, 1.0, v140
	v_sub_f32_e32 v163, 1.0, v141
	v_sub_f32_e32 v164, 1.0, v142
	v_sub_f32_e32 v165, 1.0, v143
	v_fmaak_f32 v154, v158, v154, 0xbcdac9b8
	v_fmaak_f32 v155, v159, v155, 0xbcdac9b8
	v_fmaak_f32 v156, v160, v156, 0xbcdac9b8
	v_fmaak_f32 v157, v161, v157, 0xbcdac9b8
	v_fmaak_f32 v154, v158, v154, 0x3de703be
	v_fmaak_f32 v155, v159, v155, 0x3de703be
	v_fmaak_f32 v156, v160, v156, 0x3de703be
	v_fmaak_f32 v157, v161, v157, 0x3de703be
	v_fmaak_f32 v154, v158, v154, 0xbec09330
	v_fmaak_f32 v155, v159, v155, 0xbec09330
	v_fmaak_f32 v156, v160, v156, 0xbec09330
	v_fmaak_f32 v157, v161, v157, 0xbec09330
	v_fmaak_f32 v158, v158, v154, 0x3e0375d0
	v_fmaak_f32 v159, v159, v155, 0x3e0375d0
	v_fmaak_f32 v160, v160, v156, 0x3e0375d0
	v_fmaak_f32 v161, v161, v157, 0x3e0375d0
	v_fma_f32 v154, |v132|, v158, |v132|
	v_fma_f32 v155, |v133|, v159, |v133|
	v_fma_f32 v156, |v134|, v160, |v134|
	v_fma_f32 v157, |v135|, v161, |v135|
	v_cmp_nlt_f32_e64 vcc, |v132|, 1.0
	v_cmp_nlt_f32_e64 s[30:31], |v133|, 1.0
	v_cmp_nlt_f32_e64 s[34:35], |v134|, 1.0
	v_cmp_nlt_f32_e64 s[36:37], |v135|, 1.0
	v_mul_f32_e32 v166, 0.5, v84
	v_mul_f32_e32 v167, 0.5, v85
	v_mul_f32_e32 v168, 0.5, v86
	v_mul_f32_e32 v169, 0.5, v87
	v_mul_f32_e32 v166, v166, v128
	v_mul_f32_e32 v167, v167, v129
	v_mul_f32_e32 v168, v168, v130
	v_mul_f32_e32 v169, v169, v131
	v_cndmask_b32_e64 v162, v154, v162, vcc
	v_cndmask_b32_e64 v163, v155, v163, s[30:31]
	v_cndmask_b32_e64 v164, v156, v164, s[34:35]
	v_cndmask_b32_e64 v165, v157, v165, s[36:37]
	v_bfi_b32 v162, s47, v162, v132
	v_bfi_b32 v163, s47, v163, v133
	v_bfi_b32 v164, s47, v164, v134
	v_bfi_b32 v165, s47, v165, v135
	v_add_f32_e32 v162, 1.0, v162
	v_add_f32_e32 v163, 1.0, v163
	v_add_f32_e32 v164, 1.0, v164
	v_add_f32_e32 v165, 1.0, v165
	v_mul_f32_e32 v166, v166, v162
	v_mul_f32_e32 v167, v167, v163
	v_mul_f32_e32 v168, v168, v164
	v_mul_f32_e32 v169, v169, v165
	v_mul_f32_e32 v166, v100, v166
	v_mul_f32_e32 v167, v101, v167
	v_mul_f32_e32 v168, v102, v168
	v_mul_f32_e32 v169, v103, v169
	global_store_dwordx4 v109, v[166:169], s[26:27]
	s_waitcnt vmcnt(9)
	v_lshlrev_b32_e32 v112, 2, v56
	v_lshlrev_b32_e32 v113, 2, v57
	v_lshlrev_b32_e32 v114, 2, v58
	v_lshlrev_b32_e32 v115, 2, v59
	global_load_dword v96, v112, s[28:29]
	global_load_dword v97, v113, s[28:29]
	global_load_dword v98, v114, s[28:29]
	global_load_dword v99, v115, s[28:29]
	v_add_u32_e32 v116, 0x10000, v112
	v_add_u32_e32 v117, 0x10000, v113
	v_add_u32_e32 v118, 0x10000, v114
	v_add_u32_e32 v119, 0x10000, v115
	global_load_dword v100, v116, s[28:29]
	global_load_dword v101, v117, s[28:29]
	global_load_dword v102, v118, s[28:29]
	global_load_dword v103, v119, s[28:29]
	s_waitcnt vmcnt(9)
; DI float bflo(unsigned u) { return __uint_as_float(u << 16); }
; DI float bfhi(unsigned u) { return __uint_as_float(u & 0xffff0000u); }
; DI void phase_peercoef(const Params& p, int bid, int nb) {
;     ...
;     for (int x = 0; x < 8; ++x) { const u32x2 pb = *(const u32x2*)(pd + (size_t)x * T_ * 128 + i4); d += (f32x4){bflo(pb[0]), bfhi(pb[0]), bflo(pb[1]), bfhi(pb[1])}; }
;     ...
;     for (int k = 0; k < 4; ++k) { const float dk = d[k] * uinv[e[k]]; o[k] = g[k] * 0.5f * dk * (1.f + erff(dk * 0.70710678118654752f)) * vinv[e[k]]; }
	v_lshlrev_b32_e32 v124, 16, v16
	v_and_b32_e32 v125, 0xffff0000, v16
	v_pk_add_f32 v[120:121], v[124:125], 0 op_sel_hi:[1,0]
	v_lshlrev_b32_e32 v124, 16, v18
	v_and_b32_e32 v125, 0xffff0000, v18
	v_pk_add_f32 v[120:121], v[120:121], v[124:125]
	v_lshlrev_b32_e32 v124, 16, v20
	v_and_b32_e32 v125, 0xffff0000, v20
	v_pk_add_f32 v[120:121], v[120:121], v[124:125]
	v_lshlrev_b32_e32 v124, 16, v22
	v_and_b32_e32 v125, 0xffff0000, v22
	v_pk_add_f32 v[120:121], v[120:121], v[124:125]
	v_lshlrev_b32_e32 v124, 16, v24
	v_and_b32_e32 v125, 0xffff0000, v24
	v_pk_add_f32 v[120:121], v[120:121], v[124:125]
	v_lshlrev_b32_e32 v124, 16, v26
	v_and_b32_e32 v125, 0xffff0000, v26
	v_pk_add_f32 v[120:121], v[120:121], v[124:125]
	v_lshlrev_b32_e32 v124, 16, v28
	v_and_b32_e32 v125, 0xffff0000, v28
	v_pk_add_f32 v[120:121], v[120:121], v[124:125]
	v_lshlrev_b32_e32 v124, 16, v30
	v_and_b32_e32 v125, 0xffff0000, v30
	v_pk_add_f32 v[120:121], v[120:121], v[124:125]
	v_lshlrev_b32_e32 v124, 16, v17
	v_and_b32_e32 v125, 0xffff0000, v17
	v_pk_add_f32 v[122:123], v[124:125], 0 op_sel_hi:[1,0]
	v_lshlrev_b32_e32 v124, 16, v19
	v_and_b32_e32 v125, 0xffff0000, v19
	v_pk_add_f32 v[122:123], v[122:123], v[124:125]
	v_lshlrev_b32_e32 v124, 16, v21
	v_and_b32_e32 v125, 0xffff0000, v21
	v_pk_add_f32 v[122:123], v[122:123], v[124:125]
	v_lshlrev_b32_e32 v124, 16, v23
	v_and_b32_e32 v125, 0xffff0000, v23
	v_pk_add_f32 v[122:123], v[122:123], v[124:125]
	v_lshlrev_b32_e32 v124, 16, v25
	v_and_b32_e32 v125, 0xffff0000, v25
	v_pk_add_f32 v[122:123], v[122:123], v[124:125]
	v_lshlrev_b32_e32 v124, 16, v27
	v_and_b32_e32 v125, 0xffff0000, v27
	v_pk_add_f32 v[122:123], v[122:123], v[124:125]
	v_lshlrev_b32_e32 v124, 16, v29
	v_and_b32_e32 v125, 0xffff0000, v29
	v_pk_add_f32 v[122:123], v[122:123], v[124:125]
	v_lshlrev_b32_e32 v124, 16, v31
	v_and_b32_e32 v125, 0xffff0000, v31
	v_pk_add_f32 v[122:123], v[122:123], v[124:125]
	v_mul_f32_e32 v128, v88, v120
	v_mul_f32_e32 v129, v89, v121
	v_mul_f32_e32 v130, v90, v122
	v_mul_f32_e32 v131, v91, v123
	v_mul_f32_e32 v132, 0x3f3504f3, v128
	v_mul_f32_e32 v133, 0x3f3504f3, v129
	v_mul_f32_e32 v134, 0x3f3504f3, v130
	v_mul_f32_e32 v135, 0x3f3504f3, v131
	v_fma_f32 v136, |v132|, s38, v5
	v_fma_f32 v137, |v133|, s38, v5
	v_fma_f32 v138, |v134|, s38, v5
	v_fma_f32 v139, |v135|, s38, v5
	v_fma_f32 v136, |v132|, v136, s39
	v_fma_f32 v137, |v133|, v137, s39
	v_fma_f32 v138, |v134|, v138, s39
	v_fma_f32 v139, |v135|, v139, s39
	v_fma_f32 v136, |v132|, v136, s40
	v_fma_f32 v137, |v133|, v137, s40
	v_fma_f32 v138, |v134|, v138, s40
	v_fma_f32 v139, |v135|, v139, s40
	v_fma_f32 v136, |v132|, v136, s41
	v_fma_f32 v137, |v133|, v137, s41
	v_fma_f32 v138, |v134|, v138, s41
	v_fma_f32 v139, |v135|, v139, s41
	v_fma_f32 v136, |v132|, v136, s42
	v_fma_f32 v137, |v133|, v137, s42
	v_fma_f32 v138, |v134|, v138, s42
	v_fma_f32 v139, |v135|, v139, s42
	v_fma_f32 v136, |v132|, v136, s43
	v_fma_f32 v137, |v133|, v137, s43
	v_fma_f32 v138, |v134|, v138, s43
	v_fma_f32 v139, |v135|, v139, s43
	v_fma_f32 v136, |v132|, v136, |v132|
	v_fma_f32 v137, |v133|, v137, |v133|
	v_fma_f32 v138, |v134|, v138, |v134|
	v_fma_f32 v139, |v135|, v139, |v135|
	v_mul_f32_e32 v140, 0xbfb8aa3b, v136
	v_mul_f32_e32 v141, 0xbfb8aa3b, v137
	v_mul_f32_e32 v142, 0xbfb8aa3b, v138
	v_mul_f32_e32 v143, 0xbfb8aa3b, v139
	v_fma_f32 v144, v136, s44, -v140
	v_fma_f32 v145, v137, s44, -v141
	v_fma_f32 v148, v138, s44, -v142
	v_fma_f32 v149, v139, s44, -v143
	v_rndne_f32_e32 v150, v140
	v_rndne_f32_e32 v151, v141
	v_rndne_f32_e32 v152, v142
	v_rndne_f32_e32 v153, v143
	v_fmac_f32_e32 v144, 0xb2a5705f, v136
	v_fmac_f32_e32 v145, 0xb2a5705f, v137
	v_fmac_f32_e32 v148, 0xb2a5705f, v138
	v_fmac_f32_e32 v149, 0xb2a5705f, v139
	v_sub_f32_e32 v140, v140, v150
	v_sub_f32_e32 v141, v141, v151
	v_sub_f32_e32 v142, v142, v152
	v_sub_f32_e32 v143, v143, v153
	v_add_f32_e32 v140, v140, v144
	v_add_f32_e32 v141, v141, v145
	v_add_f32_e32 v142, v142, v148
	v_add_f32_e32 v143, v143, v149
	v_cvt_i32_f32_e32 v150, v150
	v_cvt_i32_f32_e32 v151, v151
	v_cvt_i32_f32_e32 v152, v152
	v_cvt_i32_f32_e32 v153, v153
	v_exp_f32_e32 v140, v140
	v_exp_f32_e32 v141, v141
	v_exp_f32_e32 v142, v142
	v_exp_f32_e32 v143, v143
	v_cmp_nlt_f32_e64 vcc, s45, v136
	v_cmp_nlt_f32_e64 s[30:31], s45, v137
	v_cmp_nlt_f32_e64 s[34:35], s45, v138
	v_cmp_nlt_f32_e64 s[36:37], s45, v139
	v_ldexp_f32 v140, v140, v150
	v_ldexp_f32 v141, v141, v151
	v_ldexp_f32 v142, v142, v152
	v_ldexp_f32 v143, v143, v153
	v_cndmask_b32_e64 v140, 0, v140, vcc
	v_cndmask_b32_e64 v141, 0, v141, s[30:31]
	v_cndmask_b32_e64 v142, 0, v142, s[34:35]
	v_cndmask_b32_e64 v143, 0, v143, s[36:37]
	v_cmp_ngt_f32_e64 vcc, s46, v136
	v_cmp_ngt_f32_e64 s[30:31], s46, v137
	v_cmp_ngt_f32_e64 s[34:35], s46, v138
	v_cmp_ngt_f32_e64 s[36:37], s46, v139
	v_mul_f32_e32 v158, v132, v132
	v_mul_f32_e32 v159, v133, v133
	v_mul_f32_e32 v160, v134, v134
	v_mul_f32_e32 v161, v135, v135
	v_fmamk_f32 v154, v158, 0xba1345e1, v4
	v_fmamk_f32 v155, v159, 0xba1345e1, v4
	v_fmamk_f32 v156, v160, 0xba1345e1, v4
	v_fmamk_f32 v157, v161, 0xba1345e1, v4
	v_cndmask_b32_e64 v140, v6, v140, vcc
	v_cndmask_b32_e64 v141, v6, v141, s[30:31]
	v_cndmask_b32_e64 v142, v6, v142, s[34:35]
	v_cndmask_b32_e64 v143, v6, v143, s[36:37]
	v_sub_f32_e32 v162, 1.0, v140
	v_sub_f32_e32 v163, 1.0, v141
	v_sub_f32_e32 v164, 1.0, v142
	v_sub_f32_e32 v165, 1.0, v143
	v_fmaak_f32 v154, v158, v154, 0xbcdac9b8
	v_fmaak_f32 v155, v159, v155, 0xbcdac9b8
	v_fmaak_f32 v156, v160, v156, 0xbcdac9b8
	v_fmaak_f32 v157, v161, v157, 0xbcdac9b8
	v_fmaak_f32 v154, v158, v154, 0x3de703be
	v_fmaak_f32 v155, v159, v155, 0x3de703be
; DI int tidx() { int t = threadIdx.x & 255; asm volatile("" : "+v"(t)); return t; }
; DI float bflo(unsigned u) { return __uint_as_float(u << 16); }
; DI float bfhi(unsigned u) { return __uint_as_float(u & 0xffff0000u); }
; DI void phase_peercoef(const Params& p, int bid, int nb) {
;     ...
;   for (size_t i4 = ((size_t)bid * NT + tidx()) * 4; i4 < (size_t)T_ * 128; i4 += (size_t)nb * NT * 4) {
;     f32x4 d = {0.f, 0.f, 0.f, 0.f};
; #pragma unroll
;     for (int x = 0; x < 8; ++x) { const u32x2 pb = *(const u32x2*)(pd + (size_t)x * T_ * 128 + i4); d += (f32x4){bflo(pb[0]), bfhi(pb[0]), bflo(pb[1]), bfhi(pb[1])}; }
;     typedef int i32x4 __attribute__((ext_vector_type(4)));
;     const i32x4 e = *(const i32x4*)(eidx + i4); const f32x4 g = *(const f32x4*)(gate + i4);
;     f32x4 o;
; #pragma unroll
;     for (int k = 0; k < 4; ++k) { const float dk = d[k] * uinv[e[k]]; o[k] = g[k] * 0.5f * dk * (1.f + erff(dk * 0.70710678118654752f)) * vinv[e[k]]; }
;     *(f32x4*)(coef + i4) = o;
	v_fmaak_f32 v156, v160, v156, 0x3de703be
	v_fmaak_f32 v157, v161, v157, 0x3de703be
	v_fmaak_f32 v154, v158, v154, 0xbec09330
	v_fmaak_f32 v155, v159, v155, 0xbec09330
	v_fmaak_f32 v156, v160, v156, 0xbec09330
	v_fmaak_f32 v157, v161, v157, 0xbec09330
	v_fmaak_f32 v158, v158, v154, 0x3e0375d0
	v_fmaak_f32 v159, v159, v155, 0x3e0375d0
	v_fmaak_f32 v160, v160, v156, 0x3e0375d0
	v_fmaak_f32 v161, v161, v157, 0x3e0375d0
	v_fma_f32 v154, |v132|, v158, |v132|
	v_fma_f32 v155, |v133|, v159, |v133|
	v_fma_f32 v156, |v134|, v160, |v134|
	v_fma_f32 v157, |v135|, v161, |v135|
	v_cmp_nlt_f32_e64 vcc, |v132|, 1.0
	v_cmp_nlt_f32_e64 s[30:31], |v133|, 1.0
	v_cmp_nlt_f32_e64 s[34:35], |v134|, 1.0
	v_cmp_nlt_f32_e64 s[36:37], |v135|, 1.0
	v_mul_f32_e32 v166, 0.5, v36
	v_mul_f32_e32 v167, 0.5, v37
	v_mul_f32_e32 v168, 0.5, v38
	v_mul_f32_e32 v169, 0.5, v39
	v_mul_f32_e32 v166, v166, v128
	v_mul_f32_e32 v167, v167, v129
	v_mul_f32_e32 v168, v168, v130
	v_mul_f32_e32 v169, v169, v131
	v_cndmask_b32_e64 v162, v154, v162, vcc
	v_cndmask_b32_e64 v163, v155, v163, s[30:31]
	v_cndmask_b32_e64 v164, v156, v164, s[34:35]
	v_cndmask_b32_e64 v165, v157, v165, s[36:37]
	v_bfi_b32 v162, s47, v162, v132
	v_bfi_b32 v163, s47, v163, v133
	v_bfi_b32 v164, s47, v164, v134
	v_bfi_b32 v165, s47, v165, v135
	v_add_f32_e32 v162, 1.0, v162
	v_add_f32_e32 v163, 1.0, v163
	v_add_f32_e32 v164, 1.0, v164
	v_add_f32_e32 v165, 1.0, v165
	v_mul_f32_e32 v166, v166, v162
	v_mul_f32_e32 v167, v167, v163
	v_mul_f32_e32 v168, v168, v164
	v_mul_f32_e32 v169, v169, v165
	v_mul_f32_e32 v166, v92, v166
	v_mul_f32_e32 v167, v93, v167
	v_mul_f32_e32 v168, v94, v168
	v_mul_f32_e32 v169, v95, v169
	global_store_dwordx4 v107, v[166:169], s[26:27]
	s_waitcnt vmcnt(1)
	v_lshlrev_b32_e32 v124, 16, v40
	v_and_b32_e32 v125, 0xffff0000, v40
	v_pk_add_f32 v[120:121], v[124:125], 0 op_sel_hi:[1,0]
	v_lshlrev_b32_e32 v124, 16, v42
	v_and_b32_e32 v125, 0xffff0000, v42
	v_pk_add_f32 v[120:121], v[120:121], v[124:125]
	v_lshlrev_b32_e32 v124, 16, v44
	v_and_b32_e32 v125, 0xffff0000, v44
	v_pk_add_f32 v[120:121], v[120:121], v[124:125]
	v_lshlrev_b32_e32 v124, 16, v46
	v_and_b32_e32 v125, 0xffff0000, v46
	v_pk_add_f32 v[120:121], v[120:121], v[124:125]
	v_lshlrev_b32_e32 v124, 16, v48
	v_and_b32_e32 v125, 0xffff0000, v48
	v_pk_add_f32 v[120:121], v[120:121], v[124:125]
	v_lshlrev_b32_e32 v124, 16, v50
	v_and_b32_e32 v125, 0xffff0000, v50
	v_pk_add_f32 v[120:121], v[120:121], v[124:125]
	v_lshlrev_b32_e32 v124, 16, v52
	v_and_b32_e32 v125, 0xffff0000, v52
	v_pk_add_f32 v[120:121], v[120:121], v[124:125]
	v_lshlrev_b32_e32 v124, 16, v54
	v_and_b32_e32 v125, 0xffff0000, v54
	v_pk_add_f32 v[120:121], v[120:121], v[124:125]
	v_lshlrev_b32_e32 v124, 16, v41
	v_and_b32_e32 v125, 0xffff0000, v41
	v_pk_add_f32 v[122:123], v[124:125], 0 op_sel_hi:[1,0]
	v_lshlrev_b32_e32 v124, 16, v43
	v_and_b32_e32 v125, 0xffff0000, v43
	v_pk_add_f32 v[122:123], v[122:123], v[124:125]
	v_lshlrev_b32_e32 v124, 16, v45
	v_and_b32_e32 v125, 0xffff0000, v45
	v_pk_add_f32 v[122:123], v[122:123], v[124:125]
	v_lshlrev_b32_e32 v124, 16, v47
	v_and_b32_e32 v125, 0xffff0000, v47
	v_pk_add_f32 v[122:123], v[122:123], v[124:125]
	v_lshlrev_b32_e32 v124, 16, v49
	v_and_b32_e32 v125, 0xffff0000, v49
	v_pk_add_f32 v[122:123], v[122:123], v[124:125]
	v_lshlrev_b32_e32 v124, 16, v51
	v_and_b32_e32 v125, 0xffff0000, v51
	v_pk_add_f32 v[122:123], v[122:123], v[124:125]
	v_lshlrev_b32_e32 v124, 16, v53
	v_and_b32_e32 v125, 0xffff0000, v53
	v_pk_add_f32 v[122:123], v[122:123], v[124:125]
	v_lshlrev_b32_e32 v124, 16, v55
	v_and_b32_e32 v125, 0xffff0000, v55
	v_pk_add_f32 v[122:123], v[122:123], v[124:125]
	v_mul_f32_e32 v128, v96, v120
	v_mul_f32_e32 v129, v97, v121
	v_mul_f32_e32 v130, v98, v122
	v_mul_f32_e32 v131, v99, v123
	v_mul_f32_e32 v132, 0x3f3504f3, v128
	v_mul_f32_e32 v133, 0x3f3504f3, v129
	v_mul_f32_e32 v134, 0x3f3504f3, v130
	v_mul_f32_e32 v135, 0x3f3504f3, v131
	v_fma_f32 v136, |v132|, s38, v5
	v_fma_f32 v137, |v133|, s38, v5
	v_fma_f32 v138, |v134|, s38, v5
	v_fma_f32 v139, |v135|, s38, v5
	v_fma_f32 v136, |v132|, v136, s39
	v_fma_f32 v137, |v133|, v137, s39
	v_fma_f32 v138, |v134|, v138, s39
	v_fma_f32 v139, |v135|, v139, s39
	v_fma_f32 v136, |v132|, v136, s40
	v_fma_f32 v137, |v133|, v137, s40
	v_fma_f32 v138, |v134|, v138, s40
	v_fma_f32 v139, |v135|, v139, s40
	v_fma_f32 v136, |v132|, v136, s41
	v_fma_f32 v137, |v133|, v137, s41
	v_fma_f32 v138, |v134|, v138, s41
	v_fma_f32 v139, |v135|, v139, s41
	v_fma_f32 v136, |v132|, v136, s42
	v_fma_f32 v137, |v133|, v137, s42
; DI void phase_peercoef(const Params& p, int bid, int nb) {
;     ...
;     for (int k = 0; k < 4; ++k) { const float dk = d[k] * uinv[e[k]]; o[k] = g[k] * 0.5f * dk * (1.f + erff(dk * 0.70710678118654752f)) * vinv[e[k]]; }
;     *(f32x4*)(coef + i4) = o;
	v_fma_f32 v138, |v134|, v138, s42
	v_fma_f32 v139, |v135|, v139, s42
	v_fma_f32 v136, |v132|, v136, s43
	v_fma_f32 v137, |v133|, v137, s43
	v_fma_f32 v138, |v134|, v138, s43
	v_fma_f32 v139, |v135|, v139, s43
	v_fma_f32 v136, |v132|, v136, |v132|
	v_fma_f32 v137, |v133|, v137, |v133|
	v_fma_f32 v138, |v134|, v138, |v134|
	v_fma_f32 v139, |v135|, v139, |v135|
	v_mul_f32_e32 v140, 0xbfb8aa3b, v136
	v_mul_f32_e32 v141, 0xbfb8aa3b, v137
	v_mul_f32_e32 v142, 0xbfb8aa3b, v138
	v_mul_f32_e32 v143, 0xbfb8aa3b, v139
	v_fma_f32 v144, v136, s44, -v140
	v_fma_f32 v145, v137, s44, -v141
	v_fma_f32 v148, v138, s44, -v142
	v_fma_f32 v149, v139, s44, -v143
	v_rndne_f32_e32 v150, v140
	v_rndne_f32_e32 v151, v141
	v_rndne_f32_e32 v152, v142
	v_rndne_f32_e32 v153, v143
	v_fmac_f32_e32 v144, 0xb2a5705f, v136
	v_fmac_f32_e32 v145, 0xb2a5705f, v137
	v_fmac_f32_e32 v148, 0xb2a5705f, v138
	v_fmac_f32_e32 v149, 0xb2a5705f, v139
	v_sub_f32_e32 v140, v140, v150
	v_sub_f32_e32 v141, v141, v151
	v_sub_f32_e32 v142, v142, v152
	v_sub_f32_e32 v143, v143, v153
	v_add_f32_e32 v140, v140, v144
	v_add_f32_e32 v141, v141, v145
	v_add_f32_e32 v142, v142, v148
	v_add_f32_e32 v143, v143, v149
	v_cvt_i32_f32_e32 v150, v150
	v_cvt_i32_f32_e32 v151, v151
	v_cvt_i32_f32_e32 v152, v152
	v_cvt_i32_f32_e32 v153, v153
	v_exp_f32_e32 v140, v140
	v_exp_f32_e32 v141, v141
	v_exp_f32_e32 v142, v142
	v_exp_f32_e32 v143, v143
	v_cmp_nlt_f32_e64 vcc, s45, v136
	v_cmp_nlt_f32_e64 s[30:31], s45, v137
	v_cmp_nlt_f32_e64 s[34:35], s45, v138
	v_cmp_nlt_f32_e64 s[36:37], s45, v139
	v_ldexp_f32 v140, v140, v150
	v_ldexp_f32 v141, v141, v151
	v_ldexp_f32 v142, v142, v152
	v_ldexp_f32 v143, v143, v153
	v_cndmask_b32_e64 v140, 0, v140, vcc
	v_cndmask_b32_e64 v141, 0, v141, s[30:31]
	v_cndmask_b32_e64 v142, 0, v142, s[34:35]
	v_cndmask_b32_e64 v143, 0, v143, s[36:37]
	v_cmp_ngt_f32_e64 vcc, s46, v136
	v_cmp_ngt_f32_e64 s[30:31], s46, v137
	v_cmp_ngt_f32_e64 s[34:35], s46, v138
	v_cmp_ngt_f32_e64 s[36:37], s46, v139
	v_mul_f32_e32 v158, v132, v132
	v_mul_f32_e32 v159, v133, v133
	v_mul_f32_e32 v160, v134, v134
	v_mul_f32_e32 v161, v135, v135
	v_fmamk_f32 v154, v158, 0xba1345e1, v4
	v_fmamk_f32 v155, v159, 0xba1345e1, v4
	v_fmamk_f32 v156, v160, 0xba1345e1, v4
	v_fmamk_f32 v157, v161, 0xba1345e1, v4
	v_cndmask_b32_e64 v140, v6, v140, vcc
	v_cndmask_b32_e64 v141, v6, v141, s[30:31]
	v_cndmask_b32_e64 v142, v6, v142, s[34:35]
	v_cndmask_b32_e64 v143, v6, v143, s[36:37]
	v_sub_f32_e32 v162, 1.0, v140
	v_sub_f32_e32 v163, 1.0, v141
	v_sub_f32_e32 v164, 1.0, v142
	v_sub_f32_e32 v165, 1.0, v143
	v_fmaak_f32 v154, v158, v154, 0xbcdac9b8
	v_fmaak_f32 v155, v159, v155, 0xbcdac9b8
	v_fmaak_f32 v156, v160, v156, 0xbcdac9b8
	v_fmaak_f32 v157, v161, v157, 0xbcdac9b8
	v_fmaak_f32 v154, v158, v154, 0x3de703be
	v_fmaak_f32 v155, v159, v155, 0x3de703be
	v_fmaak_f32 v156, v160, v156, 0x3de703be
	v_fmaak_f32 v157, v161, v157, 0x3de703be
	v_fmaak_f32 v154, v158, v154, 0xbec09330
	v_fmaak_f32 v155, v159, v155, 0xbec09330
	v_fmaak_f32 v156, v160, v156, 0xbec09330
	v_fmaak_f32 v157, v161, v157, 0xbec09330
	v_fmaak_f32 v158, v158, v154, 0x3e0375d0
	v_fmaak_f32 v159, v159, v155, 0x3e0375d0
	v_fmaak_f32 v160, v160, v156, 0x3e0375d0
	v_fmaak_f32 v161, v161, v157, 0x3e0375d0
	v_fma_f32 v154, |v132|, v158, |v132|
	v_fma_f32 v155, |v133|, v159, |v133|
	v_fma_f32 v156, |v134|, v160, |v134|
	v_fma_f32 v157, |v135|, v161, |v135|
	v_cmp_nlt_f32_e64 vcc, |v132|, 1.0
	v_cmp_nlt_f32_e64 s[30:31], |v133|, 1.0
	v_cmp_nlt_f32_e64 s[34:35], |v134|, 1.0
	v_cmp_nlt_f32_e64 s[36:37], |v135|, 1.0
	v_mul_f32_e32 v166, 0.5, v60
	v_mul_f32_e32 v167, 0.5, v61
	v_mul_f32_e32 v168, 0.5, v62
	v_mul_f32_e32 v169, 0.5, v63
	v_mul_f32_e32 v166, v166, v128
	v_mul_f32_e32 v167, v167, v129
	v_mul_f32_e32 v168, v168, v130
	v_mul_f32_e32 v169, v169, v131
	v_cndmask_b32_e64 v162, v154, v162, vcc
	v_cndmask_b32_e64 v163, v155, v163, s[30:31]
	v_cndmask_b32_e64 v164, v156, v164, s[34:35]
	v_cndmask_b32_e64 v165, v157, v165, s[36:37]
	v_bfi_b32 v162, s47, v162, v132
	v_bfi_b32 v163, s47, v163, v133
	v_bfi_b32 v164, s47, v164, v134
	v_bfi_b32 v165, s47, v165, v135
	v_add_f32_e32 v162, 1.0, v162
	v_add_f32_e32 v163, 1.0, v163
	v_add_f32_e32 v164, 1.0, v164
	v_add_f32_e32 v165, 1.0, v165
	v_mul_f32_e32 v166, v166, v162
	v_mul_f32_e32 v167, v167, v163
	v_mul_f32_e32 v168, v168, v164
	v_mul_f32_e32 v169, v169, v165
	v_mul_f32_e32 v166, v100, v166
	v_mul_f32_e32 v167, v101, v167
	v_mul_f32_e32 v168, v102, v168
	v_mul_f32_e32 v169, v103, v169
	global_store_dwordx4 v108, v[166:169], s[26:27]
